# peel first K-loop iteration of each GEMM unit (C=0, no accumulator zeroing) + PRO weight-transpose loads issued up front
# baseline (speedup 1.0000x reference)
; #define GAS __attribute__((address_space(1)))
; #define LAS __attribute__((address_space(3)))
; #define LDS_WAIT() asm volatile("s_waitcnt lgkmcnt(0)" ::: "memory")
; __device__ __forceinline__ void p0_transpose_item(const float* W, int K, int N, bf16* WT, int drow0, int k0, int n0, const float* gain, LAS float* scr, int lane) {
; #pragma unroll 8
;     for (int i = 0; i < 32; ++i) { const int kk = 2 * i + (lane >> 5); scr[kk * 33 + (lane & 31)] = __builtin_nontemporal_load(W + (size_t)(k0 + kk) * N + n0 + (lane & 31)); }
;     LDS_WAIT(); asm volatile("" ::: "memory");
;     const int c = lane & 7;
;     f32x4 ga = {1.f, 1.f, 1.f, 1.f}, gb = ga;
;     if (gain) { ga = *(const GAS f32x4*)(gain + k0 + 8 * c); gb = *(const GAS f32x4*)(gain + k0 + 8 * c + 4); }
.LBB0_57:
	v_add_u32_e32 v6, s91, v2
	v_mad_u64_u32 v[4:5], s[92:93], v6, s97, 0
	v_add_u32_e32 v8, 2, v6
	v_add_u32_e32 v17, 4, v6
	v_add_u32_e32 v37, 6, v6
	v_ashrrev_i32_e32 v7, 31, v6
	v_add_u32_e32 v40, 8, v6
	v_add_u32_e32 v42, 10, v6
	v_add_u32_e32 v44, 12, v6
	v_add_u32_e32 v46, 14, v6
	v_mov_b32_e32 v6, v5
	v_ashrrev_i32_e32 v49, 31, v8
	v_mad_u64_u32 v[8:9], s[92:93], v8, s97, 0
	v_mad_u64_u32 v[28:29], s[92:93], v17, s97, 0
	v_mad_u64_u32 v[38:39], s[92:93], v37, s97, 0
	v_ashrrev_i32_e32 v51, 31, v17
	v_ashrrev_i32_e32 v17, 31, v37
	v_ashrrev_i32_e32 v37, 31, v40
	v_mad_u64_u32 v[40:41], s[92:93], v40, s97, 0
	v_ashrrev_i32_e32 v55, 31, v42
	v_mad_u64_u32 v[42:43], s[92:93], v42, s97, 0
	v_ashrrev_i32_e32 v57, 31, v44
	v_mad_u64_u32 v[44:45], s[92:93], v44, s97, 0
	v_ashrrev_i32_e32 v59, 31, v46
	v_mad_u64_u32 v[46:47], s[92:93], v46, s97, 0
	v_mad_u64_u32 v[6:7], s[92:93], v7, s97, v[6:7]
	v_mov_b32_e32 v48, v9
	v_mov_b32_e32 v50, v29
	v_mov_b32_e32 v52, v39
	v_mov_b32_e32 v54, v41
	v_mov_b32_e32 v56, v43
	v_mov_b32_e32 v58, v45
	v_mov_b32_e32 v60, v47
	v_mov_b32_e32 v5, v6
	v_mad_u64_u32 v[6:7], s[92:93], v49, s97, v[48:49]
	v_mad_u64_u32 v[48:49], s[92:93], v51, s97, v[50:51]
	v_mad_u64_u32 v[50:51], s[92:93], v17, s97, v[52:53]
	v_mad_u64_u32 v[52:53], s[92:93], v37, s97, v[54:55]
	v_mad_u64_u32 v[54:55], s[92:93], v55, s97, v[56:57]
	v_mad_u64_u32 v[56:57], s[92:93], v57, s97, v[58:59]
	v_mad_u64_u32 v[58:59], s[92:93], v59, s97, v[60:61]
	v_mov_b32_e32 v9, v6
	v_mov_b32_e32 v29, v48
	v_mov_b32_e32 v39, v50
	v_lshl_add_u64 v[4:5], v[4:5], 2, v[26:27]
	v_mov_b32_e32 v41, v52
	v_mov_b32_e32 v43, v54
	v_mov_b32_e32 v45, v56
	v_mov_b32_e32 v47, v58
	v_lshl_add_u64 v[6:7], v[8:9], 2, v[26:27]
	v_lshl_add_u64 v[8:9], v[28:29], 2, v[26:27]
	v_lshl_add_u64 v[28:29], v[38:39], 2, v[26:27]
	v_lshl_add_u64 v[38:39], v[40:41], 2, v[26:27]
	v_lshl_add_u64 v[40:41], v[42:43], 2, v[26:27]
	v_lshl_add_u64 v[42:43], v[44:45], 2, v[26:27]
	v_lshl_add_u64 v[44:45], v[46:47], 2, v[26:27]
	global_load_dword v64, v[4:5], off nt
	global_load_dword v65, v[6:7], off nt
	global_load_dword v66, v[8:9], off nt
	global_load_dword v67, v[28:29], off nt
	global_load_dword v68, v[38:39], off nt
	global_load_dword v69, v[40:41], off nt
	global_load_dword v70, v[42:43], off nt
	global_load_dword v71, v[44:45], off nt
	s_lshl_b32 s98, s97, 6
	s_mov_b32 s99, 0
	v_lshl_add_u64 v[4:5], v[4:5], 0, s[98:99]
	v_lshl_add_u64 v[6:7], v[6:7], 0, s[98:99]
	v_lshl_add_u64 v[8:9], v[8:9], 0, s[98:99]
	v_lshl_add_u64 v[28:29], v[28:29], 0, s[98:99]
	v_lshl_add_u64 v[38:39], v[38:39], 0, s[98:99]
	v_lshl_add_u64 v[40:41], v[40:41], 0, s[98:99]
	v_lshl_add_u64 v[42:43], v[42:43], 0, s[98:99]
	v_lshl_add_u64 v[44:45], v[44:45], 0, s[98:99]
	global_load_dword v72, v[4:5], off nt
	global_load_dword v73, v[6:7], off nt
	global_load_dword v74, v[8:9], off nt
	global_load_dword v75, v[28:29], off nt
	global_load_dword v76, v[38:39], off nt
	global_load_dword v77, v[40:41], off nt
	global_load_dword v78, v[42:43], off nt
	global_load_dword v79, v[44:45], off nt
	v_lshl_add_u64 v[4:5], v[4:5], 0, s[98:99]
	v_lshl_add_u64 v[6:7], v[6:7], 0, s[98:99]
	v_lshl_add_u64 v[8:9], v[8:9], 0, s[98:99]
	v_lshl_add_u64 v[28:29], v[28:29], 0, s[98:99]
	v_lshl_add_u64 v[38:39], v[38:39], 0, s[98:99]
	v_lshl_add_u64 v[40:41], v[40:41], 0, s[98:99]
	v_lshl_add_u64 v[42:43], v[42:43], 0, s[98:99]
	v_lshl_add_u64 v[44:45], v[44:45], 0, s[98:99]
	global_load_dword v80, v[4:5], off nt
	global_load_dword v81, v[6:7], off nt
	global_load_dword v82, v[8:9], off nt
	global_load_dword v83, v[28:29], off nt
	global_load_dword v84, v[38:39], off nt
	global_load_dword v85, v[40:41], off nt
	global_load_dword v86, v[42:43], off nt
	global_load_dword v87, v[44:45], off nt
	v_lshl_add_u64 v[4:5], v[4:5], 0, s[98:99]
	v_lshl_add_u64 v[6:7], v[6:7], 0, s[98:99]
	v_lshl_add_u64 v[8:9], v[8:9], 0, s[98:99]
	v_lshl_add_u64 v[28:29], v[28:29], 0, s[98:99]
	v_lshl_add_u64 v[38:39], v[38:39], 0, s[98:99]
	v_lshl_add_u64 v[40:41], v[40:41], 0, s[98:99]
	v_lshl_add_u64 v[42:43], v[42:43], 0, s[98:99]
	v_lshl_add_u64 v[44:45], v[44:45], 0, s[98:99]
	global_load_dword v88, v[4:5], off nt
	global_load_dword v89, v[6:7], off nt
	global_load_dword v90, v[8:9], off nt
	global_load_dword v91, v[28:29], off nt
	global_load_dword v92, v[38:39], off nt
	global_load_dword v93, v[40:41], off nt
	global_load_dword v94, v[42:43], off nt
	global_load_dword v95, v[44:45], off nt
	v_add_u32_e32 v29, 0x400, v3
	s_waitcnt vmcnt(30)
	ds_write2_b32 v3, v64, v65 offset1:66
	s_waitcnt vmcnt(28)
	ds_write2_b32 v3, v66, v67 offset0:132 offset1:198
	s_waitcnt vmcnt(26)
	ds_write2_b32 v29, v68, v69 offset0:8 offset1:74
	s_waitcnt vmcnt(24)
	ds_write2_b32 v29, v70, v71 offset0:140 offset1:206
	v_add_u32_e32 v3, 0x840, v3
	v_add_u32_e32 v29, 0x400, v3
	s_waitcnt vmcnt(22)
	ds_write2_b32 v3, v72, v73 offset1:66
	s_waitcnt vmcnt(20)
	ds_write2_b32 v3, v74, v75 offset0:132 offset1:198
	s_waitcnt vmcnt(18)
	ds_write2_b32 v29, v76, v77 offset0:8 offset1:74
	s_waitcnt vmcnt(16)
	ds_write2_b32 v29, v78, v79 offset0:140 offset1:206
	v_add_u32_e32 v3, 0x840, v3
	v_add_u32_e32 v29, 0x400, v3
	s_waitcnt vmcnt(14)
	ds_write2_b32 v3, v80, v81 offset1:66
	s_waitcnt vmcnt(12)
	ds_write2_b32 v3, v82, v83 offset0:132 offset1:198
	s_waitcnt vmcnt(10)
	ds_write2_b32 v29, v84, v85 offset0:8 offset1:74
	s_waitcnt vmcnt(8)
	ds_write2_b32 v29, v86, v87 offset0:140 offset1:206
	v_add_u32_e32 v3, 0x840, v3
	v_add_u32_e32 v29, 0x400, v3
	s_waitcnt vmcnt(6)
	ds_write2_b32 v3, v88, v89 offset1:66
	s_waitcnt vmcnt(4)
	ds_write2_b32 v3, v90, v91 offset0:132 offset1:198
	s_waitcnt vmcnt(2)
	ds_write2_b32 v29, v92, v93 offset0:8 offset1:74
	s_waitcnt vmcnt(0)
	ds_write2_b32 v29, v94, v95 offset0:140 offset1:206
	v_add_u32_e32 v3, 0x840, v3
	s_waitcnt lgkmcnt(0)
	s_ashr_i32 s91, s90, 31
	s_and_b64 vcc, exec, s[88:89]
	s_cbranch_vccz .LBB0_61
	v_lshl_add_u64 v[6:7], s[90:91], 2, v[20:21]
	global_load_dwordx4 v[2:5], v[6:7], off offset:16
	s_nop 0
	global_load_dwordx4 v[6:9], v[6:7], off
	s_waitcnt vmcnt(1)
	v_mov_b32_e32 v28, v3
	v_mov_b32_e32 v3, v4
	v_mov_b32_e32 v29, v5
	s_waitcnt vmcnt(0)
	v_mov_b32_e32 v4, v7
	v_mov_b32_e32 v7, v8
	v_mov_b32_e32 v5, v9
	s_branch .LBB0_62

; #define PG8_STAGE(bufoff, gbase, voff) do { _Pragma("unroll") for (int _i = 0; _i < 2; ++_i) \
;         __builtin_amdgcn_global_load_lds((const unsigned*)((const char*)(gbase) + (voff)[_i]), (PG8_LAS unsigned*)(lds + (bufoff) + ldsw + _i * 8192), 16, 0, 0); } while (0)
; #define PG8_LDA(dst, b, h) do { _Pragma("unroll") for (int m = 0; m < 4; ++m) Frag<F8>::load(dst[m], lds + PG8_SA(b, h) + aoff + m * 2048); } while (0)
; #define PG8_LDB(dst, b, h) do { _Pragma("unroll") for (int n = 0; n < 2; ++n) Frag<F8>::load(dst[n], lds + PG8_SB(b, h) + boff + n * 2048); } while (0)
; #define PG8_MMA(ai, bj, At, Bt) do { __builtin_amdgcn_s_setprio(3); _Pragma("unroll") for (int m = 0; m < 4; ++m) _Pragma("unroll") for (int n = 0; n < 2; ++n) Frag<F8>::mma(acc[ai][bj][m][n], Bt[n], At[m]); \
;         __builtin_amdgcn_s_setprio(0); } while (0)
; #define PG8_WAIT_V(n) asm volatile("s_waitcnt vmcnt(" #n ")" ::: "memory")
; #define PG8_WAIT_L(n) asm volatile("s_waitcnt lgkmcnt(" #n ")" ::: "memory")
; #define PG8_BAR __builtin_amdgcn_s_barrier()
; #define PG8_SCHED __builtin_amdgcn_sched_barrier(0)
; template <class Epi, class Sched, bool ALIGN_EPI = false, bool SP2 = false, bool F8 = false>
; __device__ __forceinline__ void gemm_phase(PG8_LAS unsigned char* lds, const Gemm g, const Sched& S, const Epi& E) {
;     ...
;         for (int t = 0; t < nt; t += 2) {
;             const bool last = (t == nt - 2);
;             const char* a1 = cA + (size_t)(t + 1) * kstep;
;             const char* a2 = last ? nA : cA + (size_t)(t + 2) * kstep; const char* b2 = last ? nB : cB + (size_t)(t + 2) * kstep;
;             const char* a3 = a2 + kstep; const char* b3 = b2 + kstep;
;             if (last && has_next) S.a_ready(nxt);
;             if constexpr (SP2) {
;             PG8_LDB(B0, 0, 0); PG8_LDB(B1, 0, 1); PG8_SCHED; PG8_LDA(At, 0, 0); PG8_STAGE(PG8_SA(1, 1), a1 + hstep, voffA);
;             PG8_WAIT_V(8); PG8_WAIT_L(0); PG8_BAR; PG8_MMA(0, 0, At, B0); PG8_MMA(0, 1, At, B1); PG8_BAR; PG8_SCHED;
;             PG8_LDA(At, 0, 1); PG8_STAGE(PG8_SB(0, 0), b2, voffB); PG8_STAGE(PG8_SB(0, 1), b2 + hstep, voffB); PG8_STAGE(PG8_SA(0, 0), a2, voffA);
;             PG8_WAIT_V(8); PG8_WAIT_L(0); PG8_BAR; PG8_MMA(1, 0, At, B0); PG8_MMA(1, 1, At, B1); PG8_BAR; PG8_SCHED;
.LBB0_150:
	s_ashr_i32 s25, s24, 31
	s_lshl_b64 s[4:5], s[24:25], 18
	s_add_u32 s38, s77, s4
	s_addc_u32 s39, s78, s5
	s_and_b64 s[4:5], s[8:9], exec
	s_cselect_b32 s25, s39, s71
	s_cselect_b32 s91, s38, s70
	s_ashr_i32 s31, s30, 31
	s_lshl_b64 s[4:5], s[30:31], 18
	s_add_u32 s42, s79, s4
	s_addc_u32 s43, s80, s5
	s_and_b64 s[4:5], s[8:9], exec
	s_cselect_b32 s31, s43, s73
	s_cselect_b32 s92, s42, s72
	s_add_u32 s70, s70, 0x20080
	s_addc_u32 s71, s71, 0
	s_add_u32 s93, s72, 0x100
	s_addc_u32 s95, s73, 0
	s_mov_b32 s96, -2
	ds_read_b128 v[18:21], v194
	ds_read_b128 v[22:25], v194 offset:1024
	ds_read_b128 v[26:29], v194 offset:2048
	ds_read_b128 v[30:33], v194 offset:3072
	ds_read_b128 v[2:5], v195
	ds_read_b128 v[6:9], v195 offset:1024
	ds_read_b128 v[10:13], v195 offset:2048
	ds_read_b128 v[14:17], v195 offset:3072
	s_add_u32 s0, s70, 0xfffe0080
	s_addc_u32 s1, s71, -1
	s_cmp_eq_u32 s96, 4
	s_cselect_b32 s75, s25, s1
	s_cselect_b32 s74, s91, s0
	s_cselect_b32 s73, s31, s95
	s_cselect_b32 s72, s92, s93
	v_lshl_add_u64 v[224:225], s[70:71], 0, v[174:175]
	s_add_i32 m0, s45, 0xc000
	ds_read_b128 v[182:185], v196
	ds_read_b128 v[186:189], v196 offset:1024
	ds_read_b128 v[200:203], v196 offset:2048
	ds_read_b128 v[204:207], v196 offset:3072
	ds_read_b128 v[208:211], v196 offset:4096
	ds_read_b128 v[212:215], v196 offset:5120
	ds_read_b128 v[216:219], v196 offset:6144
	ds_read_b128 v[220:223], v196 offset:7168
	global_load_lds_dwordx4 v[224:225], off
	v_lshl_add_u64 v[224:225], s[70:71], 0, v[176:177]
	s_add_i32 m0, s45, 0xe000
	s_nop 0
	global_load_lds_dwordx4 v[224:225], off
	s_waitcnt vmcnt(8)
	s_waitcnt lgkmcnt(0)
	s_barrier
	s_setprio 3
	s_waitcnt lgkmcnt(0)
	v_mfma_scale_f32_16x16x128_f8f6f4 v[158:161], v[18:25], v[182:189], 0, v197, v197 op_sel_hi:[0, 0, 0]
	v_mfma_scale_f32_16x16x128_f8f6f4 v[154:157], v[26:33], v[182:189], 0, v197, v197 op_sel_hi:[0, 0, 0]
	v_mfma_scale_f32_16x16x128_f8f6f4 v[150:153], v[18:25], v[200:207], 0, v197, v197 op_sel_hi:[0, 0, 0]
	v_mfma_scale_f32_16x16x128_f8f6f4 v[142:145], v[26:33], v[200:207], 0, v197, v197 op_sel_hi:[0, 0, 0]
	v_mfma_scale_f32_16x16x128_f8f6f4 v[130:133], v[18:25], v[208:215], 0, v197, v197 op_sel_hi:[0, 0, 0]
	v_mfma_scale_f32_16x16x128_f8f6f4 v[122:125], v[26:33], v[208:215], 0, v197, v197 op_sel_hi:[0, 0, 0]
	v_mfma_scale_f32_16x16x128_f8f6f4 v[118:121], v[18:25], v[216:223], 0, v197, v197 op_sel_hi:[0, 0, 0]
	v_mfma_scale_f32_16x16x128_f8f6f4 v[110:113], v[26:33], v[216:223], 0, v197, v197 op_sel_hi:[0, 0, 0]
	s_setprio 0
	s_setprio 3
	v_mfma_scale_f32_16x16x128_f8f6f4 v[146:149], v[2:9], v[182:189], 0, v197, v197 op_sel_hi:[0, 0, 0]
	v_mfma_scale_f32_16x16x128_f8f6f4 v[138:141], v[10:17], v[182:189], 0, v197, v197 op_sel_hi:[0, 0, 0]
	v_mfma_scale_f32_16x16x128_f8f6f4 v[134:137], v[2:9], v[200:207], 0, v197, v197 op_sel_hi:[0, 0, 0]
	v_mfma_scale_f32_16x16x128_f8f6f4 v[126:129], v[10:17], v[200:207], 0, v197, v197 op_sel_hi:[0, 0, 0]
	v_mfma_scale_f32_16x16x128_f8f6f4 v[114:117], v[2:9], v[208:215], 0, v197, v197 op_sel_hi:[0, 0, 0]
	v_mfma_scale_f32_16x16x128_f8f6f4 v[106:109], v[10:17], v[208:215], 0, v197, v197 op_sel_hi:[0, 0, 0]
	v_mfma_scale_f32_16x16x128_f8f6f4 v[102:105], v[2:9], v[216:223], 0, v197, v197 op_sel_hi:[0, 0, 0]
	v_mfma_scale_f32_16x16x128_f8f6f4 v[98:101], v[10:17], v[216:223], 0, v197, v197 op_sel_hi:[0, 0, 0]
	s_setprio 0
	s_barrier
	s_add_i32 s0, s87, s76
	v_lshl_add_u64 v[182:183], s[72:73], 0, v[170:171]
	s_mov_b32 m0, s0
	ds_read_b128 v[200:203], v196 offset:16384
	ds_read_b128 v[204:207], v196 offset:17408
	ds_read_b128 v[208:211], v196 offset:18432
	ds_read_b128 v[212:215], v196 offset:19456
	ds_read_b128 v[216:219], v196 offset:20480
	ds_read_b128 v[220:223], v196 offset:21504
	ds_read_b128 v[224:227], v196 offset:22528
	ds_read_b128 v[228:231], v196 offset:23552
	global_load_lds_dwordx4 v[182:183], off
	s_add_i32 m0, s0, 0x2000
	s_add_u32 s4, s72, 0x20000
	v_lshl_add_u64 v[184:185], s[72:73], 0, v[166:167]
	s_addc_u32 s5, s73, 0
	s_add_i32 s0, s88, s76
	global_load_lds_dwordx4 v[184:185], off
	v_lshl_add_u64 v[186:187], s[4:5], 0, v[170:171]
	s_mov_b32 m0, s0
	v_lshl_add_u64 v[188:189], s[74:75], 0, v[168:169]
	global_load_lds_dwordx4 v[186:187], off
	v_lshl_add_u64 v[186:187], s[4:5], 0, v[166:167]
	s_add_i32 m0, s0, 0x2000
	s_nop 0
	global_load_lds_dwordx4 v[186:187], off
	v_lshl_add_u64 v[186:187], s[74:75], 0, v[172:173]
	s_mov_b32 m0, s45
	s_nop 0
	global_load_lds_dwordx4 v[186:187], off
	s_mov_b32 m0, s82
	s_nop 0
	global_load_lds_dwordx4 v[188:189], off
	s_waitcnt vmcnt(8)
	s_waitcnt lgkmcnt(0)
	s_barrier
	s_setprio 3
	s_waitcnt lgkmcnt(0)
	v_mfma_scale_f32_16x16x128_f8f6f4 v[94:97], v[18:25], v[200:207], 0, v197, v197 op_sel_hi:[0, 0, 0]
	v_mfma_scale_f32_16x16x128_f8f6f4 v[90:93], v[26:33], v[200:207], 0, v197, v197 op_sel_hi:[0, 0, 0]
	v_mfma_scale_f32_16x16x128_f8f6f4 v[86:89], v[18:25], v[208:215], 0, v197, v197 op_sel_hi:[0, 0, 0]
	v_mfma_scale_f32_16x16x128_f8f6f4 v[82:85], v[26:33], v[208:215], 0, v197, v197 op_sel_hi:[0, 0, 0]
	v_mfma_scale_f32_16x16x128_f8f6f4 v[70:73], v[18:25], v[216:223], 0, v197, v197 op_sel_hi:[0, 0, 0]
	v_mfma_scale_f32_16x16x128_f8f6f4 v[66:69], v[26:33], v[216:223], 0, v197, v197 op_sel_hi:[0, 0, 0]
	v_mfma_scale_f32_16x16x128_f8f6f4 v[54:57], v[18:25], v[224:231], 0, v197, v197 op_sel_hi:[0, 0, 0]
	v_mfma_scale_f32_16x16x128_f8f6f4 v[50:53], v[26:33], v[224:231], 0, v197, v197 op_sel_hi:[0, 0, 0]
	s_setprio 0
	s_setprio 3
	v_mfma_scale_f32_16x16x128_f8f6f4 v[78:81], v[2:9], v[200:207], 0, v197, v197 op_sel_hi:[0, 0, 0]
	v_mfma_scale_f32_16x16x128_f8f6f4 v[74:77], v[10:17], v[200:207], 0, v197, v197 op_sel_hi:[0, 0, 0]
	v_mfma_scale_f32_16x16x128_f8f6f4 v[62:65], v[2:9], v[208:215], 0, v197, v197 op_sel_hi:[0, 0, 0]
	v_mfma_scale_f32_16x16x128_f8f6f4 v[58:61], v[10:17], v[208:215], 0, v197, v197 op_sel_hi:[0, 0, 0]
	v_mfma_scale_f32_16x16x128_f8f6f4 v[46:49], v[2:9], v[216:223], 0, v197, v197 op_sel_hi:[0, 0, 0]
	v_mfma_scale_f32_16x16x128_f8f6f4 v[42:45], v[10:17], v[216:223], 0, v197, v197 op_sel_hi:[0, 0, 0]
	v_mfma_scale_f32_16x16x128_f8f6f4 v[38:41], v[2:9], v[224:231], 0, v197, v197 op_sel_hi:[0, 0, 0]
	v_mfma_scale_f32_16x16x128_f8f6f4 v[34:37], v[10:17], v[224:231], 0, v197, v197 op_sel_hi:[0, 0, 0]
	s_setprio 0
	s_barrier
; #define PG8_STAGE(bufoff, gbase, voff) do { _Pragma("unroll") for (int _i = 0; _i < 2; ++_i) \
;         __builtin_amdgcn_global_load_lds((const unsigned*)((const char*)(gbase) + (voff)[_i]), (PG8_LAS unsigned*)(lds + (bufoff) + ldsw + _i * 8192), 16, 0, 0); } while (0)
; #define PG8_LDA(dst, b, h) do { _Pragma("unroll") for (int m = 0; m < 4; ++m) Frag<F8>::load(dst[m], lds + PG8_SA(b, h) + aoff + m * 2048); } while (0)
; #define PG8_LDB(dst, b, h) do { _Pragma("unroll") for (int n = 0; n < 2; ++n) Frag<F8>::load(dst[n], lds + PG8_SB(b, h) + boff + n * 2048); } while (0)
; #define PG8_MMA(ai, bj, At, Bt) do { __builtin_amdgcn_s_setprio(3); _Pragma("unroll") for (int m = 0; m < 4; ++m) _Pragma("unroll") for (int n = 0; n < 2; ++n) Frag<F8>::mma(acc[ai][bj][m][n], Bt[n], At[m]); \
;         __builtin_amdgcn_s_setprio(0); } while (0)
; #define PG8_WAIT_V(n) asm volatile("s_waitcnt vmcnt(" #n ")" ::: "memory")
; #define PG8_WAIT_L(n) asm volatile("s_waitcnt lgkmcnt(" #n ")" ::: "memory")
; #define PG8_BAR __builtin_amdgcn_s_barrier()
; #define PG8_SCHED __builtin_amdgcn_sched_barrier(0)
; template <class Epi, class Sched, bool ALIGN_EPI = false, bool SP2 = false, bool F8 = false>
; __device__ __forceinline__ void gemm_phase(PG8_LAS unsigned char* lds, const Gemm g, const Sched& S, const Epi& E) {
;     ...
;             PG8_LDB(B0, 1, 0); PG8_LDB(B1, 1, 1); PG8_SCHED; PG8_LDA(At, 1, 0); PG8_STAGE(PG8_SA(0, 1), a2 + hstep, voffA);
;             PG8_WAIT_V(8); PG8_WAIT_L(0); PG8_BAR; PG8_MMA(0, 0, At, B0); PG8_MMA(0, 1, At, B1); PG8_BAR; PG8_SCHED;
;             PG8_LDA(At, 1, 1); PG8_STAGE(PG8_SB(1, 0), b3, voffB); PG8_STAGE(PG8_SB(1, 1), b3 + hstep, voffB); PG8_STAGE(PG8_SA(1, 0), a3, voffA);
;             PG8_WAIT_V(8); PG8_WAIT_L(0); PG8_BAR; PG8_MMA(1, 0, At, B0); PG8_MMA(1, 1, At, B1); PG8_BAR; PG8_SCHED;
	s_add_i32 s0, 0, 0x18000
	s_add_i32 s1, 0, 0x1c000
	v_add_u32_e32 v14, s0, v190
	v_add_u32_e32 v30, s1, v190
	ds_read_b128 v[2:5], v14
	ds_read_b128 v[6:9], v14 offset:1024
	ds_read_b128 v[10:13], v14 offset:2048
	ds_read_b128 v[14:17], v14 offset:3072
	ds_read_b128 v[18:21], v30
	ds_read_b128 v[22:25], v30 offset:1024
	ds_read_b128 v[26:29], v30 offset:2048
	ds_read_b128 v[30:33], v30 offset:3072
	s_add_u32 s4, s74, 0x20000
	s_addc_u32 s5, s75, 0
	s_mov_b32 m0, s83
	v_lshl_add_u64 v[232:233], s[4:5], 0, v[172:173]
	ds_read_b128 v[200:203], v196 offset:32768
	ds_read_b128 v[204:207], v196 offset:33792
	ds_read_b128 v[208:211], v196 offset:34816
	ds_read_b128 v[212:215], v196 offset:35840
	ds_read_b128 v[216:219], v196 offset:36864
	ds_read_b128 v[220:223], v196 offset:37888
	ds_read_b128 v[224:227], v196 offset:38912
	ds_read_b128 v[228:231], v196 offset:39936
	global_load_lds_dwordx4 v[232:233], off
	v_lshl_add_u64 v[232:233], s[4:5], 0, v[168:169]
	s_mov_b32 m0, s84
	s_nop 0
	global_load_lds_dwordx4 v[232:233], off
	s_waitcnt vmcnt(8)
	s_waitcnt lgkmcnt(0)
	s_barrier
	s_setprio 3
	s_waitcnt lgkmcnt(0)
	v_mfma_scale_f32_16x16x128_f8f6f4 v[158:161], v[2:9], v[200:207], v[158:161], v197, v197 op_sel_hi:[0,0,0]
	v_mfma_scale_f32_16x16x128_f8f6f4 v[154:157], v[10:17], v[200:207], v[154:157], v197, v197 op_sel_hi:[0,0,0]
	v_mfma_scale_f32_16x16x128_f8f6f4 v[150:153], v[2:9], v[208:215], v[150:153], v197, v197 op_sel_hi:[0,0,0]
	v_mfma_scale_f32_16x16x128_f8f6f4 v[142:145], v[10:17], v[208:215], v[142:145], v197, v197 op_sel_hi:[0,0,0]
	v_mfma_scale_f32_16x16x128_f8f6f4 v[130:133], v[2:9], v[216:223], v[130:133], v197, v197 op_sel_hi:[0,0,0]
	v_mfma_scale_f32_16x16x128_f8f6f4 v[122:125], v[10:17], v[216:223], v[122:125], v197, v197 op_sel_hi:[0,0,0]
	v_mfma_scale_f32_16x16x128_f8f6f4 v[118:121], v[2:9], v[224:231], v[118:121], v197, v197 op_sel_hi:[0,0,0]
	v_mfma_scale_f32_16x16x128_f8f6f4 v[110:113], v[10:17], v[224:231], v[110:113], v197, v197 op_sel_hi:[0,0,0]
	s_setprio 0
	s_setprio 3
	v_mfma_scale_f32_16x16x128_f8f6f4 v[146:149], v[18:25], v[200:207], v[146:149], v197, v197 op_sel_hi:[0,0,0]
	v_mfma_scale_f32_16x16x128_f8f6f4 v[138:141], v[26:33], v[200:207], v[138:141], v197, v197 op_sel_hi:[0,0,0]
	v_mfma_scale_f32_16x16x128_f8f6f4 v[134:137], v[18:25], v[208:215], v[134:137], v197, v197 op_sel_hi:[0,0,0]
	v_mfma_scale_f32_16x16x128_f8f6f4 v[126:129], v[26:33], v[208:215], v[126:129], v197, v197 op_sel_hi:[0,0,0]
	v_mfma_scale_f32_16x16x128_f8f6f4 v[114:117], v[18:25], v[216:223], v[114:117], v197, v197 op_sel_hi:[0,0,0]
	v_mfma_scale_f32_16x16x128_f8f6f4 v[106:109], v[26:33], v[216:223], v[106:109], v197, v197 op_sel_hi:[0,0,0]
	v_mfma_scale_f32_16x16x128_f8f6f4 v[102:105], v[18:25], v[224:231], v[102:105], v197, v197 op_sel_hi:[0,0,0]
	v_mfma_scale_f32_16x16x128_f8f6f4 v[98:101], v[26:33], v[224:231], v[98:101], v197, v197 op_sel_hi:[0,0,0]
	s_setprio 0
	s_barrier
	s_add_i32 s0, s0, s76
	v_lshl_add_u64 v[182:183], v[182:183], 0, s[18:19]
	s_mov_b32 m0, s0
	ds_read_b128 v[200:203], v196 offset:49152
	ds_read_b128 v[204:207], v196 offset:50176
	ds_read_b128 v[208:211], v196 offset:51200
	ds_read_b128 v[212:215], v196 offset:52224
	ds_read_b128 v[216:219], v196 offset:53248
	ds_read_b128 v[220:223], v196 offset:54272
	ds_read_b128 v[224:227], v196 offset:55296
	ds_read_b128 v[228:231], v196 offset:56320
	global_load_lds_dwordx4 v[182:183], off
	s_add_i32 m0, s0, 0x2000
	s_add_u32 s4, s72, 0x20080
	v_lshl_add_u64 v[182:183], v[184:185], 0, s[18:19]
	s_addc_u32 s5, s73, 0
	s_add_i32 s0, s1, s76
	global_load_lds_dwordx4 v[182:183], off
	v_lshl_add_u64 v[182:183], s[4:5], 0, v[170:171]
	s_mov_b32 m0, s0
	s_nop 0
	global_load_lds_dwordx4 v[182:183], off
	v_lshl_add_u64 v[182:183], s[4:5], 0, v[166:167]
	s_add_i32 m0, s0, 0x2000
	s_nop 0
	global_load_lds_dwordx4 v[182:183], off
	v_lshl_add_u64 v[182:183], v[186:187], 0, s[18:19]
	s_mov_b32 m0, s85
	s_nop 0
	global_load_lds_dwordx4 v[182:183], off
	v_lshl_add_u64 v[182:183], v[188:189], 0, s[18:19]
	s_mov_b32 m0, s86
	s_nop 0
	global_load_lds_dwordx4 v[182:183], off
	s_waitcnt vmcnt(8)
	s_waitcnt lgkmcnt(0)
	s_barrier
	s_setprio 3
	s_waitcnt lgkmcnt(0)
	v_mfma_scale_f32_16x16x128_f8f6f4 v[94:97], v[2:9], v[200:207], v[94:97], v197, v197 op_sel_hi:[0,0,0]
	v_mfma_scale_f32_16x16x128_f8f6f4 v[90:93], v[10:17], v[200:207], v[90:93], v197, v197 op_sel_hi:[0,0,0]
	v_mfma_scale_f32_16x16x128_f8f6f4 v[86:89], v[2:9], v[208:215], v[86:89], v197, v197 op_sel_hi:[0,0,0]
	v_mfma_scale_f32_16x16x128_f8f6f4 v[82:85], v[10:17], v[208:215], v[82:85], v197, v197 op_sel_hi:[0,0,0]
	v_mfma_scale_f32_16x16x128_f8f6f4 v[70:73], v[2:9], v[216:223], v[70:73], v197, v197 op_sel_hi:[0,0,0]
	v_mfma_scale_f32_16x16x128_f8f6f4 v[66:69], v[10:17], v[216:223], v[66:69], v197, v197 op_sel_hi:[0,0,0]
	v_mfma_scale_f32_16x16x128_f8f6f4 v[54:57], v[2:9], v[224:231], v[54:57], v197, v197 op_sel_hi:[0,0,0]
	v_mfma_scale_f32_16x16x128_f8f6f4 v[50:53], v[10:17], v[224:231], v[50:53], v197, v197 op_sel_hi:[0,0,0]
	s_setprio 0
	s_setprio 3
	v_mfma_scale_f32_16x16x128_f8f6f4 v[78:81], v[18:25], v[200:207], v[78:81], v197, v197 op_sel_hi:[0,0,0]
	v_mfma_scale_f32_16x16x128_f8f6f4 v[74:77], v[26:33], v[200:207], v[74:77], v197, v197 op_sel_hi:[0,0,0]
	v_mfma_scale_f32_16x16x128_f8f6f4 v[62:65], v[18:25], v[208:215], v[62:65], v197, v197 op_sel_hi:[0,0,0]
	v_mfma_scale_f32_16x16x128_f8f6f4 v[58:61], v[26:33], v[208:215], v[58:61], v197, v197 op_sel_hi:[0,0,0]
	v_mfma_scale_f32_16x16x128_f8f6f4 v[46:49], v[18:25], v[216:223], v[46:49], v197, v197 op_sel_hi:[0,0,0]
	v_mfma_scale_f32_16x16x128_f8f6f4 v[42:45], v[26:33], v[216:223], v[42:45], v197, v197 op_sel_hi:[0,0,0]
	v_mfma_scale_f32_16x16x128_f8f6f4 v[38:41], v[18:25], v[224:231], v[38:41], v197, v197 op_sel_hi:[0,0,0]
	v_mfma_scale_f32_16x16x128_f8f6f4 v[34:37], v[26:33], v[224:231], v[34:37], v197, v197 op_sel_hi:[0,0,0]
	s_setprio 0
	s_barrier
	s_add_i32 s96, s96, 2
	s_add_u32 s70, s70, 0x100
	s_addc_u32 s71, s71, 0
	s_add_u32 s93, s93, 0x100
	s_addc_u32 s95, s95, 0
	s_cmp_gt_u32 s96, 5
	s_cbranch_scc1 .Lpeel_exit_0

; #define PG8_BAR __builtin_amdgcn_s_barrier()
; #define PG8_SCHED __builtin_amdgcn_sched_barrier(0)
; template <class Epi, class Sched, bool ALIGN_EPI = false, bool SP2 = false, bool F8 = false>
; __device__ __forceinline__ void gemm_phase(PG8_LAS unsigned char* lds, const Gemm g, const Sched& S, const Epi& E) {
;     ...
;         }
;         if constexpr (ALIGN_EPI) { if (wr == 0) PG8_BAR; }
;         if constexpr (F8) { asm volatile("s_nop 15\n\ts_nop 15" ::: "memory"); PG8_SCHED; }
;         if constexpr (!Epi::AFTER_DRAIN) { E(acc, cur, wr, wc, fr, fq); S.done(cur); }
.Lpeel_exit_0:
	s_and_b64 vcc, exec, s[22:23]
	s_cbranch_vccz .LBB0_154
	s_barrier

; #define PG8_STAGE(bufoff, gbase, voff) do { _Pragma("unroll") for (int _i = 0; _i < 2; ++_i) \
;         __builtin_amdgcn_global_load_lds((const unsigned*)((const char*)(gbase) + (voff)[_i]), (PG8_LAS unsigned*)(lds + (bufoff) + ldsw + _i * 8192), 16, 0, 0); } while (0)
; #define PG8_LDA(dst, b, h) do { _Pragma("unroll") for (int m = 0; m < 4; ++m) Frag<F8>::load(dst[m], lds + PG8_SA(b, h) + aoff + m * 2048); } while (0)
; #define PG8_LDB(dst, b, h) do { _Pragma("unroll") for (int n = 0; n < 2; ++n) Frag<F8>::load(dst[n], lds + PG8_SB(b, h) + boff + n * 2048); } while (0)
; #define PG8_MMA(ai, bj, At, Bt) do { __builtin_amdgcn_s_setprio(3); _Pragma("unroll") for (int m = 0; m < 4; ++m) _Pragma("unroll") for (int n = 0; n < 2; ++n) Frag<F8>::mma(acc[ai][bj][m][n], Bt[n], At[m]); \
;         __builtin_amdgcn_s_setprio(0); } while (0)
; #define PG8_WAIT_V(n) asm volatile("s_waitcnt vmcnt(" #n ")" ::: "memory")
; #define PG8_WAIT_L(n) asm volatile("s_waitcnt lgkmcnt(" #n ")" ::: "memory")
; #define PG8_BAR __builtin_amdgcn_s_barrier()
; #define PG8_SCHED __builtin_amdgcn_sched_barrier(0)
; template <class Epi, class Sched, bool ALIGN_EPI = false, bool SP2 = false, bool F8 = false>
; __device__ __forceinline__ void gemm_phase(PG8_LAS unsigned char* lds, const Gemm g, const Sched& S, const Epi& E) {
;     ...
;         for (int t = 0; t < nt; t += 2) {
;             const bool last = (t == nt - 2);
;             const char* a1 = cA + (size_t)(t + 1) * kstep;
;             const char* a2 = last ? nA : cA + (size_t)(t + 2) * kstep; const char* b2 = last ? nB : cB + (size_t)(t + 2) * kstep;
;             const char* a3 = a2 + kstep; const char* b3 = b2 + kstep;
;             if (last && has_next) S.a_ready(nxt);
;             if constexpr (SP2) {
;             PG8_LDB(B0, 0, 0); PG8_LDB(B1, 0, 1); PG8_SCHED; PG8_LDA(At, 0, 0); PG8_STAGE(PG8_SA(1, 1), a1 + hstep, voffA);
;             PG8_WAIT_V(8); PG8_WAIT_L(0); PG8_BAR; PG8_MMA(0, 0, At, B0); PG8_MMA(0, 1, At, B1); PG8_BAR; PG8_SCHED;
;             PG8_LDA(At, 0, 1); PG8_STAGE(PG8_SB(0, 0), b2, voffB); PG8_STAGE(PG8_SB(0, 1), b2 + hstep, voffB); PG8_STAGE(PG8_SA(0, 0), a2, voffA);
;             PG8_WAIT_V(8); PG8_WAIT_L(0); PG8_BAR; PG8_MMA(1, 0, At, B0); PG8_MMA(1, 1, At, B1); PG8_BAR; PG8_SCHED;
.LBB0_561:
	s_ashr_i32 s25, s24, 31
	s_lshl_b64 s[4:5], s[24:25], 19
	s_add_u32 s36, s50, s4
	s_addc_u32 s37, s51, s5
	s_and_b64 s[4:5], s[8:9], exec
	s_cselect_b32 s6, s37, s43
	s_cselect_b32 s7, s36, s42
	s_ashr_i32 s31, s30, 31
	s_lshl_b64 s[4:5], s[30:31], 19
	s_add_u32 s38, s52, s4
	s_addc_u32 s39, s53, s5
	s_and_b64 s[4:5], s[8:9], exec
	s_cselect_b32 s25, s39, s45
	s_cselect_b32 s31, s38, s44
	s_add_u32 s42, s42, 0x40080
	s_addc_u32 s43, s43, 0
	s_add_u32 s84, s44, 0x100
	s_addc_u32 s85, s45, 0
	s_mov_b32 s86, -2
	ds_read_b128 v[146:149], v155
	ds_read_b128 v[158:161], v155 offset:1024
	ds_read_b128 v[166:169], v155 offset:2048
	ds_read_b128 v[170:173], v155 offset:3072
	ds_read_b128 v[174:177], v156
	ds_read_b128 v[178:181], v156 offset:1024
	ds_read_b128 v[182:185], v156 offset:2048
	ds_read_b128 v[186:189], v156 offset:3072
	s_add_u32 s0, s42, 0xfffc0080
	s_addc_u32 s1, s43, -1
	s_cmp_eq_u32 s86, 12
	s_cselect_b32 s47, s6, s1
	s_cselect_b32 s46, s7, s0
	s_cselect_b32 s45, s25, s85
	s_cselect_b32 s44, s31, s84
	v_lshl_add_u64 v[222:223], s[42:43], 0, v[138:139]
	s_add_i32 m0, s41, 0xc000
	ds_read_b128 v[190:193], v157
	ds_read_b128 v[194:197], v157 offset:1024
	ds_read_b128 v[198:201], v157 offset:2048
	ds_read_b128 v[202:205], v157 offset:3072
	ds_read_b128 v[206:209], v157 offset:4096
	ds_read_b128 v[210:213], v157 offset:5120
	ds_read_b128 v[214:217], v157 offset:6144
	ds_read_b128 v[218:221], v157 offset:7168
	global_load_lds_dwordx4 v[222:223], off
	v_lshl_add_u64 v[222:223], s[42:43], 0, v[140:141]
	s_add_i32 m0, s41, 0xe000
	s_nop 0
	global_load_lds_dwordx4 v[222:223], off
	s_waitcnt vmcnt(8)
	s_waitcnt lgkmcnt(0)
	s_barrier
	s_setprio 3
	s_waitcnt lgkmcnt(0)
	v_mfma_f32_16x16x32_bf16 v[126:129], v[146:149], v[190:193], 0
	v_mfma_f32_16x16x32_bf16 v[118:121], v[166:169], v[190:193], 0
	v_mfma_f32_16x16x32_bf16 v[110:113], v[146:149], v[198:201], 0
	v_mfma_f32_16x16x32_bf16 v[102:105], v[166:169], v[198:201], 0
	v_mfma_f32_16x16x32_bf16 v[94:97], v[146:149], v[206:209], 0
	v_mfma_f32_16x16x32_bf16 v[86:89], v[166:169], v[206:209], 0
	v_mfma_f32_16x16x32_bf16 v[78:81], v[146:149], v[214:217], 0
	v_mfma_f32_16x16x32_bf16 v[70:73], v[166:169], v[214:217], 0
	v_mfma_f32_16x16x32_bf16 v[126:129], v[158:161], v[194:197], v[126:129]
	v_mfma_f32_16x16x32_bf16 v[118:121], v[170:173], v[194:197], v[118:121]
	v_mfma_f32_16x16x32_bf16 v[110:113], v[158:161], v[202:205], v[110:113]
	v_mfma_f32_16x16x32_bf16 v[102:105], v[170:173], v[202:205], v[102:105]
	v_mfma_f32_16x16x32_bf16 v[94:97], v[158:161], v[210:213], v[94:97]
	v_mfma_f32_16x16x32_bf16 v[86:89], v[170:173], v[210:213], v[86:89]
	v_mfma_f32_16x16x32_bf16 v[78:81], v[158:161], v[218:221], v[78:81]
	v_mfma_f32_16x16x32_bf16 v[70:73], v[170:173], v[218:221], v[70:73]
	s_setprio 0
	s_setprio 3
	v_mfma_f32_16x16x32_bf16 v[122:125], v[174:177], v[190:193], 0
	v_mfma_f32_16x16x32_bf16 v[114:117], v[182:185], v[190:193], 0
	v_mfma_f32_16x16x32_bf16 v[106:109], v[174:177], v[198:201], 0
	v_mfma_f32_16x16x32_bf16 v[98:101], v[182:185], v[198:201], 0
	v_mfma_f32_16x16x32_bf16 v[90:93], v[174:177], v[206:209], 0
	v_mfma_f32_16x16x32_bf16 v[82:85], v[182:185], v[206:209], 0
	v_mfma_f32_16x16x32_bf16 v[74:77], v[174:177], v[214:217], 0
	v_mfma_f32_16x16x32_bf16 v[66:69], v[182:185], v[214:217], 0
	v_mfma_f32_16x16x32_bf16 v[122:125], v[178:181], v[194:197], v[122:125]
	v_mfma_f32_16x16x32_bf16 v[114:117], v[186:189], v[194:197], v[114:117]
	v_mfma_f32_16x16x32_bf16 v[106:109], v[178:181], v[202:205], v[106:109]
	v_mfma_f32_16x16x32_bf16 v[98:101], v[186:189], v[202:205], v[98:101]
	v_mfma_f32_16x16x32_bf16 v[90:93], v[178:181], v[210:213], v[90:93]
	v_mfma_f32_16x16x32_bf16 v[82:85], v[186:189], v[210:213], v[82:85]
	v_mfma_f32_16x16x32_bf16 v[74:77], v[178:181], v[218:221], v[74:77]
	v_mfma_f32_16x16x32_bf16 v[66:69], v[186:189], v[218:221], v[66:69]
	s_setprio 0
	s_barrier
	s_add_i32 s0, s80, s49
	v_lshl_add_u64 v[222:223], s[44:45], 0, v[134:135]
	s_mov_b32 m0, s0
	ds_read_b128 v[190:193], v157 offset:16384
	ds_read_b128 v[194:197], v157 offset:17408
	ds_read_b128 v[198:201], v157 offset:18432
	ds_read_b128 v[202:205], v157 offset:19456
	ds_read_b128 v[206:209], v157 offset:20480
	ds_read_b128 v[210:213], v157 offset:21504
	ds_read_b128 v[214:217], v157 offset:22528
	ds_read_b128 v[218:221], v157 offset:23552
	global_load_lds_dwordx4 v[222:223], off
	s_add_i32 m0, s0, 0x2000
	s_add_u32 s4, s44, 0x40000
	v_lshl_add_u64 v[224:225], s[44:45], 0, v[130:131]
	s_addc_u32 s5, s45, 0
	s_add_i32 s0, s81, s49
	global_load_lds_dwordx4 v[224:225], off
	v_lshl_add_u64 v[226:227], s[4:5], 0, v[134:135]
	s_mov_b32 m0, s0
	v_lshl_add_u64 v[228:229], s[46:47], 0, v[132:133]
	global_load_lds_dwordx4 v[226:227], off
	v_lshl_add_u64 v[226:227], s[4:5], 0, v[130:131]
	s_add_i32 m0, s0, 0x2000
	s_nop 0
	global_load_lds_dwordx4 v[226:227], off
	v_lshl_add_u64 v[226:227], s[46:47], 0, v[136:137]
	s_mov_b32 m0, s41
	s_nop 0
	global_load_lds_dwordx4 v[226:227], off
	s_mov_b32 m0, s72
	s_nop 0
	global_load_lds_dwordx4 v[228:229], off
	s_waitcnt vmcnt(8)
	s_waitcnt lgkmcnt(0)
	s_barrier
; #define PG8_STAGE(bufoff, gbase, voff) do { _Pragma("unroll") for (int _i = 0; _i < 2; ++_i) \
;         __builtin_amdgcn_global_load_lds((const unsigned*)((const char*)(gbase) + (voff)[_i]), (PG8_LAS unsigned*)(lds + (bufoff) + ldsw + _i * 8192), 16, 0, 0); } while (0)
; #define PG8_LDA(dst, b, h) do { _Pragma("unroll") for (int m = 0; m < 4; ++m) Frag<F8>::load(dst[m], lds + PG8_SA(b, h) + aoff + m * 2048); } while (0)
; #define PG8_LDB(dst, b, h) do { _Pragma("unroll") for (int n = 0; n < 2; ++n) Frag<F8>::load(dst[n], lds + PG8_SB(b, h) + boff + n * 2048); } while (0)
; #define PG8_MMA(ai, bj, At, Bt) do { __builtin_amdgcn_s_setprio(3); _Pragma("unroll") for (int m = 0; m < 4; ++m) _Pragma("unroll") for (int n = 0; n < 2; ++n) Frag<F8>::mma(acc[ai][bj][m][n], Bt[n], At[m]); \
;         __builtin_amdgcn_s_setprio(0); } while (0)
; #define PG8_WAIT_V(n) asm volatile("s_waitcnt vmcnt(" #n ")" ::: "memory")
; #define PG8_WAIT_L(n) asm volatile("s_waitcnt lgkmcnt(" #n ")" ::: "memory")
; #define PG8_BAR __builtin_amdgcn_s_barrier()
; #define PG8_SCHED __builtin_amdgcn_sched_barrier(0)
; template <class Epi, class Sched, bool ALIGN_EPI = false, bool SP2 = false, bool F8 = false>
; __device__ __forceinline__ void gemm_phase(PG8_LAS unsigned char* lds, const Gemm g, const Sched& S, const Epi& E) {
;     ...
;             PG8_WAIT_V(8); PG8_WAIT_L(0); PG8_BAR; PG8_MMA(1, 0, At, B0); PG8_MMA(1, 1, At, B1); PG8_BAR; PG8_SCHED;
;             PG8_LDB(B0, 1, 0); PG8_LDB(B1, 1, 1); PG8_SCHED; PG8_LDA(At, 1, 0); PG8_STAGE(PG8_SA(0, 1), a2 + hstep, voffA);
;             PG8_WAIT_V(8); PG8_WAIT_L(0); PG8_BAR; PG8_MMA(0, 0, At, B0); PG8_MMA(0, 1, At, B1); PG8_BAR; PG8_SCHED;
	s_setprio 3
	s_waitcnt lgkmcnt(0)
	v_mfma_f32_16x16x32_bf16 v[62:65], v[146:149], v[190:193], 0
	v_mfma_f32_16x16x32_bf16 v[58:61], v[166:169], v[190:193], 0
	v_mfma_f32_16x16x32_bf16 v[50:53], v[146:149], v[198:201], 0
	v_mfma_f32_16x16x32_bf16 v[42:45], v[166:169], v[198:201], 0
	v_mfma_f32_16x16x32_bf16 v[34:37], v[146:149], v[206:209], 0
	v_mfma_f32_16x16x32_bf16 v[26:29], v[166:169], v[206:209], 0
	v_mfma_f32_16x16x32_bf16 v[14:17], v[146:149], v[214:217], 0
	v_mfma_f32_16x16x32_bf16 v[6:9], v[166:169], v[214:217], 0
	v_mfma_f32_16x16x32_bf16 v[62:65], v[158:161], v[194:197], v[62:65]
	v_mfma_f32_16x16x32_bf16 v[58:61], v[170:173], v[194:197], v[58:61]
	v_mfma_f32_16x16x32_bf16 v[50:53], v[158:161], v[202:205], v[50:53]
	v_mfma_f32_16x16x32_bf16 v[42:45], v[170:173], v[202:205], v[42:45]
	v_mfma_f32_16x16x32_bf16 v[34:37], v[158:161], v[210:213], v[34:37]
	v_mfma_f32_16x16x32_bf16 v[26:29], v[170:173], v[210:213], v[26:29]
	v_mfma_f32_16x16x32_bf16 v[14:17], v[158:161], v[218:221], v[14:17]
	v_mfma_f32_16x16x32_bf16 v[6:9], v[170:173], v[218:221], v[6:9]
	s_setprio 0
	s_setprio 3
	v_mfma_f32_16x16x32_bf16 v[54:57], v[174:177], v[190:193], 0
	v_mfma_f32_16x16x32_bf16 v[46:49], v[182:185], v[190:193], 0
	v_mfma_f32_16x16x32_bf16 v[38:41], v[174:177], v[198:201], 0
	v_mfma_f32_16x16x32_bf16 v[30:33], v[182:185], v[198:201], 0
	v_mfma_f32_16x16x32_bf16 v[22:25], v[174:177], v[206:209], 0
	v_mfma_f32_16x16x32_bf16 v[18:21], v[182:185], v[206:209], 0
	v_mfma_f32_16x16x32_bf16 v[10:13], v[174:177], v[214:217], 0
	v_mfma_f32_16x16x32_bf16 v[2:5], v[182:185], v[214:217], 0
	v_mfma_f32_16x16x32_bf16 v[54:57], v[178:181], v[194:197], v[54:57]
	v_mfma_f32_16x16x32_bf16 v[46:49], v[186:189], v[194:197], v[46:49]
	v_mfma_f32_16x16x32_bf16 v[38:41], v[178:181], v[202:205], v[38:41]
	v_mfma_f32_16x16x32_bf16 v[30:33], v[186:189], v[202:205], v[30:33]
	v_mfma_f32_16x16x32_bf16 v[22:25], v[178:181], v[210:213], v[22:25]
	v_mfma_f32_16x16x32_bf16 v[18:21], v[186:189], v[210:213], v[18:21]
	v_mfma_f32_16x16x32_bf16 v[10:13], v[178:181], v[218:221], v[10:13]
	v_mfma_f32_16x16x32_bf16 v[2:5], v[186:189], v[218:221], v[2:5]
	s_setprio 0
	s_barrier
	s_add_i32 s0, 0, 0x18000
	v_add_u32_e32 v165, s0, v151
	s_add_i32 s1, 0, 0x1c000
	ds_read_b128 v[146:149], v165
	ds_read_b128 v[158:161], v165 offset:1024
	ds_read_b128 v[166:169], v165 offset:2048
	ds_read_b128 v[170:173], v165 offset:3072
	v_add_u32_e32 v165, s1, v151
	ds_read_b128 v[174:177], v165
	ds_read_b128 v[178:181], v165 offset:1024
	ds_read_b128 v[182:185], v165 offset:2048
	ds_read_b128 v[186:189], v165 offset:3072
	s_add_u32 s4, s46, 0x40000
	s_addc_u32 s5, s47, 0
	s_mov_b32 m0, s73
	v_lshl_add_u64 v[230:231], s[4:5], 0, v[136:137]
	ds_read_b128 v[190:193], v157 offset:32768
	ds_read_b128 v[194:197], v157 offset:33792
	ds_read_b128 v[198:201], v157 offset:34816
	ds_read_b128 v[202:205], v157 offset:35840
	ds_read_b128 v[206:209], v157 offset:36864
	ds_read_b128 v[210:213], v157 offset:37888
	ds_read_b128 v[214:217], v157 offset:38912
	ds_read_b128 v[218:221], v157 offset:39936
	global_load_lds_dwordx4 v[230:231], off
	v_lshl_add_u64 v[230:231], s[4:5], 0, v[132:133]
	s_mov_b32 m0, s74
	s_nop 0
	global_load_lds_dwordx4 v[230:231], off
	s_waitcnt vmcnt(8)
	s_waitcnt lgkmcnt(0)
	s_barrier
	s_setprio 3
	s_waitcnt lgkmcnt(0)
	v_mfma_f32_16x16x32_bf16 v[126:129], v[146:149], v[190:193], v[126:129]
	v_mfma_f32_16x16x32_bf16 v[118:121], v[166:169], v[190:193], v[118:121]
	v_mfma_f32_16x16x32_bf16 v[110:113], v[146:149], v[198:201], v[110:113]
	v_mfma_f32_16x16x32_bf16 v[102:105], v[166:169], v[198:201], v[102:105]
	v_mfma_f32_16x16x32_bf16 v[94:97], v[146:149], v[206:209], v[94:97]
	v_mfma_f32_16x16x32_bf16 v[86:89], v[166:169], v[206:209], v[86:89]
	v_mfma_f32_16x16x32_bf16 v[78:81], v[146:149], v[214:217], v[78:81]
	v_mfma_f32_16x16x32_bf16 v[70:73], v[166:169], v[214:217], v[70:73]
	v_mfma_f32_16x16x32_bf16 v[126:129], v[158:161], v[194:197], v[126:129]
	v_mfma_f32_16x16x32_bf16 v[118:121], v[170:173], v[194:197], v[118:121]
	v_mfma_f32_16x16x32_bf16 v[110:113], v[158:161], v[202:205], v[110:113]
	v_mfma_f32_16x16x32_bf16 v[102:105], v[170:173], v[202:205], v[102:105]
	v_mfma_f32_16x16x32_bf16 v[94:97], v[158:161], v[210:213], v[94:97]
	v_mfma_f32_16x16x32_bf16 v[86:89], v[170:173], v[210:213], v[86:89]
	v_mfma_f32_16x16x32_bf16 v[78:81], v[158:161], v[218:221], v[78:81]
	v_mfma_f32_16x16x32_bf16 v[70:73], v[170:173], v[218:221], v[70:73]
	s_setprio 0
	s_setprio 3
	v_mfma_f32_16x16x32_bf16 v[122:125], v[174:177], v[190:193], v[122:125]
	v_mfma_f32_16x16x32_bf16 v[114:117], v[182:185], v[190:193], v[114:117]
	v_mfma_f32_16x16x32_bf16 v[106:109], v[174:177], v[198:201], v[106:109]
	v_mfma_f32_16x16x32_bf16 v[98:101], v[182:185], v[198:201], v[98:101]
	v_mfma_f32_16x16x32_bf16 v[90:93], v[174:177], v[206:209], v[90:93]
	v_mfma_f32_16x16x32_bf16 v[82:85], v[182:185], v[206:209], v[82:85]
	v_mfma_f32_16x16x32_bf16 v[74:77], v[174:177], v[214:217], v[74:77]
	v_mfma_f32_16x16x32_bf16 v[66:69], v[182:185], v[214:217], v[66:69]
	v_mfma_f32_16x16x32_bf16 v[122:125], v[178:181], v[194:197], v[122:125]
	v_mfma_f32_16x16x32_bf16 v[114:117], v[186:189], v[194:197], v[114:117]
	v_mfma_f32_16x16x32_bf16 v[106:109], v[178:181], v[202:205], v[106:109]
	v_mfma_f32_16x16x32_bf16 v[98:101], v[186:189], v[202:205], v[98:101]
	v_mfma_f32_16x16x32_bf16 v[90:93], v[178:181], v[210:213], v[90:93]
	v_mfma_f32_16x16x32_bf16 v[82:85], v[186:189], v[210:213], v[82:85]
	v_mfma_f32_16x16x32_bf16 v[74:77], v[178:181], v[218:221], v[74:77]
	v_mfma_f32_16x16x32_bf16 v[66:69], v[186:189], v[218:221], v[66:69]
	s_setprio 0
	s_barrier
; #define PG8_STAGE(bufoff, gbase, voff) do { _Pragma("unroll") for (int _i = 0; _i < 2; ++_i) \
;         __builtin_amdgcn_global_load_lds((const unsigned*)((const char*)(gbase) + (voff)[_i]), (PG8_LAS unsigned*)(lds + (bufoff) + ldsw + _i * 8192), 16, 0, 0); } while (0)
; #define PG8_LDA(dst, b, h) do { _Pragma("unroll") for (int m = 0; m < 4; ++m) Frag<F8>::load(dst[m], lds + PG8_SA(b, h) + aoff + m * 2048); } while (0)
; #define PG8_MMA(ai, bj, At, Bt) do { __builtin_amdgcn_s_setprio(3); _Pragma("unroll") for (int m = 0; m < 4; ++m) _Pragma("unroll") for (int n = 0; n < 2; ++n) Frag<F8>::mma(acc[ai][bj][m][n], Bt[n], At[m]); \
;         __builtin_amdgcn_s_setprio(0); } while (0)
; #define PG8_WAIT_V(n) asm volatile("s_waitcnt vmcnt(" #n ")" ::: "memory")
; #define PG8_WAIT_L(n) asm volatile("s_waitcnt lgkmcnt(" #n ")" ::: "memory")
; #define PG8_BAR __builtin_amdgcn_s_barrier()
; #define PG8_SCHED __builtin_amdgcn_sched_barrier(0)
; template <class Epi, class Sched, bool ALIGN_EPI = false, bool SP2 = false, bool F8 = false>
; __device__ __forceinline__ void gemm_phase(PG8_LAS unsigned char* lds, const Gemm g, const Sched& S, const Epi& E) {
;     ...
;             PG8_LDA(At, 1, 1); PG8_STAGE(PG8_SB(1, 0), b3, voffB); PG8_STAGE(PG8_SB(1, 1), b3 + hstep, voffB); PG8_STAGE(PG8_SA(1, 0), a3, voffA);
;             PG8_WAIT_V(8); PG8_WAIT_L(0); PG8_BAR; PG8_MMA(1, 0, At, B0); PG8_MMA(1, 1, At, B1); PG8_BAR; PG8_SCHED;
	s_add_i32 s0, s0, s49
	v_lshl_add_u64 v[222:223], v[222:223], 0, s[18:19]
	s_mov_b32 m0, s0
	ds_read_b128 v[190:193], v157 offset:49152
	ds_read_b128 v[194:197], v157 offset:50176
	ds_read_b128 v[198:201], v157 offset:51200
	ds_read_b128 v[202:205], v157 offset:52224
	ds_read_b128 v[206:209], v157 offset:53248
	ds_read_b128 v[210:213], v157 offset:54272
	ds_read_b128 v[214:217], v157 offset:55296
	ds_read_b128 v[218:221], v157 offset:56320
	global_load_lds_dwordx4 v[222:223], off
	s_add_i32 m0, s0, 0x2000
	s_add_u32 s4, s44, 0x40080
	v_lshl_add_u64 v[222:223], v[224:225], 0, s[18:19]
	s_addc_u32 s5, s45, 0
	s_add_i32 s0, s1, s49
	global_load_lds_dwordx4 v[222:223], off
	v_lshl_add_u64 v[222:223], s[4:5], 0, v[134:135]
	s_mov_b32 m0, s0
	s_nop 0
	global_load_lds_dwordx4 v[222:223], off
	v_lshl_add_u64 v[222:223], s[4:5], 0, v[130:131]
	s_add_i32 m0, s0, 0x2000
	s_nop 0
	global_load_lds_dwordx4 v[222:223], off
	v_lshl_add_u64 v[222:223], v[226:227], 0, s[18:19]
	s_mov_b32 m0, s75
	s_nop 0
	global_load_lds_dwordx4 v[222:223], off
	v_lshl_add_u64 v[222:223], v[228:229], 0, s[18:19]
	s_mov_b32 m0, s79
	s_nop 0
	global_load_lds_dwordx4 v[222:223], off
	s_waitcnt vmcnt(8)
	s_waitcnt lgkmcnt(0)
	s_barrier
	s_setprio 3
	s_waitcnt lgkmcnt(0)
	v_mfma_f32_16x16x32_bf16 v[62:65], v[146:149], v[190:193], v[62:65]
	v_mfma_f32_16x16x32_bf16 v[58:61], v[166:169], v[190:193], v[58:61]
	v_mfma_f32_16x16x32_bf16 v[50:53], v[146:149], v[198:201], v[50:53]
	v_mfma_f32_16x16x32_bf16 v[42:45], v[166:169], v[198:201], v[42:45]
	v_mfma_f32_16x16x32_bf16 v[34:37], v[146:149], v[206:209], v[34:37]
	v_mfma_f32_16x16x32_bf16 v[26:29], v[166:169], v[206:209], v[26:29]
	v_mfma_f32_16x16x32_bf16 v[14:17], v[146:149], v[214:217], v[14:17]
	v_mfma_f32_16x16x32_bf16 v[6:9], v[166:169], v[214:217], v[6:9]
	v_mfma_f32_16x16x32_bf16 v[62:65], v[158:161], v[194:197], v[62:65]
	v_mfma_f32_16x16x32_bf16 v[58:61], v[170:173], v[194:197], v[58:61]
	v_mfma_f32_16x16x32_bf16 v[50:53], v[158:161], v[202:205], v[50:53]
	v_mfma_f32_16x16x32_bf16 v[42:45], v[170:173], v[202:205], v[42:45]
	v_mfma_f32_16x16x32_bf16 v[34:37], v[158:161], v[210:213], v[34:37]
	v_mfma_f32_16x16x32_bf16 v[26:29], v[170:173], v[210:213], v[26:29]
	v_mfma_f32_16x16x32_bf16 v[14:17], v[158:161], v[218:221], v[14:17]
	v_mfma_f32_16x16x32_bf16 v[6:9], v[170:173], v[218:221], v[6:9]
	s_setprio 0
	s_setprio 3
	v_mfma_f32_16x16x32_bf16 v[54:57], v[174:177], v[190:193], v[54:57]
	v_mfma_f32_16x16x32_bf16 v[46:49], v[182:185], v[190:193], v[46:49]
	v_mfma_f32_16x16x32_bf16 v[38:41], v[174:177], v[198:201], v[38:41]
	v_mfma_f32_16x16x32_bf16 v[30:33], v[182:185], v[198:201], v[30:33]
	v_mfma_f32_16x16x32_bf16 v[22:25], v[174:177], v[206:209], v[22:25]
	v_mfma_f32_16x16x32_bf16 v[18:21], v[182:185], v[206:209], v[18:21]
	v_mfma_f32_16x16x32_bf16 v[10:13], v[174:177], v[214:217], v[10:13]
	v_mfma_f32_16x16x32_bf16 v[2:5], v[182:185], v[214:217], v[2:5]
	v_mfma_f32_16x16x32_bf16 v[54:57], v[178:181], v[194:197], v[54:57]
	v_mfma_f32_16x16x32_bf16 v[46:49], v[186:189], v[194:197], v[46:49]
	v_mfma_f32_16x16x32_bf16 v[38:41], v[178:181], v[202:205], v[38:41]
	v_mfma_f32_16x16x32_bf16 v[30:33], v[186:189], v[202:205], v[30:33]
	v_mfma_f32_16x16x32_bf16 v[22:25], v[178:181], v[210:213], v[22:25]
	v_mfma_f32_16x16x32_bf16 v[18:21], v[186:189], v[210:213], v[18:21]
	v_mfma_f32_16x16x32_bf16 v[10:13], v[178:181], v[218:221], v[10:13]
	v_mfma_f32_16x16x32_bf16 v[2:5], v[186:189], v[218:221], v[2:5]
	s_setprio 0
	s_barrier
	s_add_i32 s86, s86, 2
	s_add_u32 s42, s42, 0x100
	s_addc_u32 s43, s43, 0
	s_add_u32 s84, s84, 0x100
	s_addc_u32 s85, s85, 0
	s_cmp_gt_u32 s86, 13
	s_cbranch_scc1 .Lpeel_exit_1

; #define PG8_STAGE(bufoff, gbase, voff) do { _Pragma("unroll") for (int _i = 0; _i < 2; ++_i) \
;         __builtin_amdgcn_global_load_lds((const unsigned*)((const char*)(gbase) + (voff)[_i]), (PG8_LAS unsigned*)(lds + (bufoff) + ldsw + _i * 8192), 16, 0, 0); } while (0)
; #define PG8_LDA(dst, b, h) do { _Pragma("unroll") for (int m = 0; m < 4; ++m) Frag<F8>::load(dst[m], lds + PG8_SA(b, h) + aoff + m * 2048); } while (0)
; #define PG8_LDB(dst, b, h) do { _Pragma("unroll") for (int n = 0; n < 2; ++n) Frag<F8>::load(dst[n], lds + PG8_SB(b, h) + boff + n * 2048); } while (0)
; #define PG8_MMA(ai, bj, At, Bt) do { __builtin_amdgcn_s_setprio(3); _Pragma("unroll") for (int m = 0; m < 4; ++m) _Pragma("unroll") for (int n = 0; n < 2; ++n) Frag<F8>::mma(acc[ai][bj][m][n], Bt[n], At[m]); \
;         __builtin_amdgcn_s_setprio(0); } while (0)
; #define PG8_WAIT_V(n) asm volatile("s_waitcnt vmcnt(" #n ")" ::: "memory")
; #define PG8_WAIT_L(n) asm volatile("s_waitcnt lgkmcnt(" #n ")" ::: "memory")
; #define PG8_BAR __builtin_amdgcn_s_barrier()
; #define PG8_SCHED __builtin_amdgcn_sched_barrier(0)
; template <class Epi, class Sched, bool ALIGN_EPI = false, bool SP2 = false, bool F8 = false>
; __device__ __forceinline__ void gemm_phase(PG8_LAS unsigned char* lds, const Gemm g, const Sched& S, const Epi& E) {
;     ...
;         for (int t = 0; t < nt; t += 2) {
;             const bool last = (t == nt - 2);
;             const char* a1 = cA + (size_t)(t + 1) * kstep;
;             const char* a2 = last ? nA : cA + (size_t)(t + 2) * kstep; const char* b2 = last ? nB : cB + (size_t)(t + 2) * kstep;
;             const char* a3 = a2 + kstep; const char* b3 = b2 + kstep;
;             if (last && has_next) S.a_ready(nxt);
;             if constexpr (SP2) {
;             PG8_LDB(B0, 0, 0); PG8_LDB(B1, 0, 1); PG8_SCHED; PG8_LDA(At, 0, 0); PG8_STAGE(PG8_SA(1, 1), a1 + hstep, voffA);
;             PG8_WAIT_V(8); PG8_WAIT_L(0); PG8_BAR; PG8_MMA(0, 0, At, B0); PG8_MMA(0, 1, At, B1); PG8_BAR; PG8_SCHED;
;             PG8_LDA(At, 0, 1); PG8_STAGE(PG8_SB(0, 0), b2, voffB); PG8_STAGE(PG8_SB(0, 1), b2 + hstep, voffB); PG8_STAGE(PG8_SA(0, 0), a2, voffA);
;             PG8_WAIT_V(8); PG8_WAIT_L(0); PG8_BAR; PG8_MMA(1, 0, At, B0); PG8_MMA(1, 1, At, B1); PG8_BAR; PG8_SCHED;
.LBB0_801:
	s_ashr_i32 s25, s24, 31
	s_lshl_b64 s[4:5], s[24:25], 18
	s_add_u32 s36, s49, s4
	s_addc_u32 s37, s50, s5
	s_and_b64 s[4:5], s[8:9], exec
	s_cselect_b32 s25, s37, s43
	s_cselect_b32 s83, s36, s42
	s_ashr_i32 s31, s30, 31
	s_lshl_b64 s[4:5], s[30:31], 18
	s_add_u32 s38, s51, s4
	s_addc_u32 s39, s52, s5
	s_and_b64 s[4:5], s[8:9], exec
	s_cselect_b32 s31, s39, s45
	s_cselect_b32 s84, s38, s44
	s_add_u32 s42, s42, 0x20080
	s_addc_u32 s43, s43, 0
	s_add_u32 s85, s44, 0x100
	s_addc_u32 s86, s45, 0
	s_mov_b32 s87, -2
	ds_read_b128 v[18:21], v194
	ds_read_b128 v[22:25], v194 offset:1024
	ds_read_b128 v[26:29], v194 offset:2048
	ds_read_b128 v[30:33], v194 offset:3072
	ds_read_b128 v[2:5], v195
	ds_read_b128 v[6:9], v195 offset:1024
	ds_read_b128 v[10:13], v195 offset:2048
	ds_read_b128 v[14:17], v195 offset:3072
	s_add_u32 s0, s42, 0xfffe0080
	s_addc_u32 s1, s43, -1
	s_cmp_eq_u32 s87, 4
	s_cselect_b32 s47, s25, s1
	s_cselect_b32 s46, s83, s0
	s_cselect_b32 s45, s31, s86
	s_cselect_b32 s44, s84, s85
	v_lshl_add_u64 v[224:225], s[42:43], 0, v[174:175]
	s_add_i32 m0, s41, 0xc000
	ds_read_b128 v[182:185], v196
	ds_read_b128 v[186:189], v196 offset:1024
	ds_read_b128 v[200:203], v196 offset:2048
	ds_read_b128 v[204:207], v196 offset:3072
	ds_read_b128 v[208:211], v196 offset:4096
	ds_read_b128 v[212:215], v196 offset:5120
	ds_read_b128 v[216:219], v196 offset:6144
	ds_read_b128 v[220:223], v196 offset:7168
	global_load_lds_dwordx4 v[224:225], off
	v_lshl_add_u64 v[224:225], s[42:43], 0, v[176:177]
	s_add_i32 m0, s41, 0xe000
	s_nop 0
	global_load_lds_dwordx4 v[224:225], off
	s_waitcnt vmcnt(8)
	s_waitcnt lgkmcnt(0)
	s_barrier
	s_setprio 3
	s_waitcnt lgkmcnt(0)
	v_mfma_scale_f32_16x16x128_f8f6f4 v[158:161], v[18:25], v[182:189], 0, v197, v197 op_sel_hi:[0, 0, 0]
	v_mfma_scale_f32_16x16x128_f8f6f4 v[154:157], v[26:33], v[182:189], 0, v197, v197 op_sel_hi:[0, 0, 0]
	v_mfma_scale_f32_16x16x128_f8f6f4 v[150:153], v[18:25], v[200:207], 0, v197, v197 op_sel_hi:[0, 0, 0]
	v_mfma_scale_f32_16x16x128_f8f6f4 v[142:145], v[26:33], v[200:207], 0, v197, v197 op_sel_hi:[0, 0, 0]
	v_mfma_scale_f32_16x16x128_f8f6f4 v[130:133], v[18:25], v[208:215], 0, v197, v197 op_sel_hi:[0, 0, 0]
	v_mfma_scale_f32_16x16x128_f8f6f4 v[122:125], v[26:33], v[208:215], 0, v197, v197 op_sel_hi:[0, 0, 0]
	v_mfma_scale_f32_16x16x128_f8f6f4 v[118:121], v[18:25], v[216:223], 0, v197, v197 op_sel_hi:[0, 0, 0]
	v_mfma_scale_f32_16x16x128_f8f6f4 v[110:113], v[26:33], v[216:223], 0, v197, v197 op_sel_hi:[0, 0, 0]
	s_setprio 0
	s_setprio 3
	v_mfma_scale_f32_16x16x128_f8f6f4 v[146:149], v[2:9], v[182:189], 0, v197, v197 op_sel_hi:[0, 0, 0]
	v_mfma_scale_f32_16x16x128_f8f6f4 v[138:141], v[10:17], v[182:189], 0, v197, v197 op_sel_hi:[0, 0, 0]
	v_mfma_scale_f32_16x16x128_f8f6f4 v[134:137], v[2:9], v[200:207], 0, v197, v197 op_sel_hi:[0, 0, 0]
	v_mfma_scale_f32_16x16x128_f8f6f4 v[126:129], v[10:17], v[200:207], 0, v197, v197 op_sel_hi:[0, 0, 0]
	v_mfma_scale_f32_16x16x128_f8f6f4 v[114:117], v[2:9], v[208:215], 0, v197, v197 op_sel_hi:[0, 0, 0]
	v_mfma_scale_f32_16x16x128_f8f6f4 v[106:109], v[10:17], v[208:215], 0, v197, v197 op_sel_hi:[0, 0, 0]
	v_mfma_scale_f32_16x16x128_f8f6f4 v[102:105], v[2:9], v[216:223], 0, v197, v197 op_sel_hi:[0, 0, 0]
	v_mfma_scale_f32_16x16x128_f8f6f4 v[98:101], v[10:17], v[216:223], 0, v197, v197 op_sel_hi:[0, 0, 0]
	s_setprio 0
	s_barrier
	s_add_i32 s0, s79, s48
	v_lshl_add_u64 v[182:183], s[44:45], 0, v[170:171]
	s_mov_b32 m0, s0
	ds_read_b128 v[200:203], v196 offset:16384
	ds_read_b128 v[204:207], v196 offset:17408
	ds_read_b128 v[208:211], v196 offset:18432
	ds_read_b128 v[212:215], v196 offset:19456
	ds_read_b128 v[216:219], v196 offset:20480
	ds_read_b128 v[220:223], v196 offset:21504
	ds_read_b128 v[224:227], v196 offset:22528
	ds_read_b128 v[228:231], v196 offset:23552
	global_load_lds_dwordx4 v[182:183], off
	s_add_i32 m0, s0, 0x2000
	s_add_u32 s4, s44, 0x20000
	v_lshl_add_u64 v[184:185], s[44:45], 0, v[166:167]
	s_addc_u32 s5, s45, 0
	s_add_i32 s0, s80, s48
	global_load_lds_dwordx4 v[184:185], off
	v_lshl_add_u64 v[186:187], s[4:5], 0, v[170:171]
	s_mov_b32 m0, s0
	v_lshl_add_u64 v[188:189], s[46:47], 0, v[168:169]
	global_load_lds_dwordx4 v[186:187], off
	v_lshl_add_u64 v[186:187], s[4:5], 0, v[166:167]
	s_add_i32 m0, s0, 0x2000
	s_nop 0
	global_load_lds_dwordx4 v[186:187], off
	v_lshl_add_u64 v[186:187], s[46:47], 0, v[172:173]
	s_mov_b32 m0, s41
	s_nop 0
	global_load_lds_dwordx4 v[186:187], off
	s_mov_b32 m0, s71
	s_nop 0
	global_load_lds_dwordx4 v[188:189], off
	s_waitcnt vmcnt(8)
	s_waitcnt lgkmcnt(0)
	s_barrier
	s_setprio 3
	s_waitcnt lgkmcnt(0)
	v_mfma_scale_f32_16x16x128_f8f6f4 v[94:97], v[18:25], v[200:207], 0, v197, v197 op_sel_hi:[0, 0, 0]
	v_mfma_scale_f32_16x16x128_f8f6f4 v[90:93], v[26:33], v[200:207], 0, v197, v197 op_sel_hi:[0, 0, 0]
	v_mfma_scale_f32_16x16x128_f8f6f4 v[86:89], v[18:25], v[208:215], 0, v197, v197 op_sel_hi:[0, 0, 0]
	v_mfma_scale_f32_16x16x128_f8f6f4 v[82:85], v[26:33], v[208:215], 0, v197, v197 op_sel_hi:[0, 0, 0]
	v_mfma_scale_f32_16x16x128_f8f6f4 v[70:73], v[18:25], v[216:223], 0, v197, v197 op_sel_hi:[0, 0, 0]
	v_mfma_scale_f32_16x16x128_f8f6f4 v[66:69], v[26:33], v[216:223], 0, v197, v197 op_sel_hi:[0, 0, 0]
	v_mfma_scale_f32_16x16x128_f8f6f4 v[54:57], v[18:25], v[224:231], 0, v197, v197 op_sel_hi:[0, 0, 0]
	v_mfma_scale_f32_16x16x128_f8f6f4 v[50:53], v[26:33], v[224:231], 0, v197, v197 op_sel_hi:[0, 0, 0]
	s_setprio 0
	s_setprio 3
	v_mfma_scale_f32_16x16x128_f8f6f4 v[78:81], v[2:9], v[200:207], 0, v197, v197 op_sel_hi:[0, 0, 0]
	v_mfma_scale_f32_16x16x128_f8f6f4 v[74:77], v[10:17], v[200:207], 0, v197, v197 op_sel_hi:[0, 0, 0]
	v_mfma_scale_f32_16x16x128_f8f6f4 v[62:65], v[2:9], v[208:215], 0, v197, v197 op_sel_hi:[0, 0, 0]
	v_mfma_scale_f32_16x16x128_f8f6f4 v[58:61], v[10:17], v[208:215], 0, v197, v197 op_sel_hi:[0, 0, 0]
	v_mfma_scale_f32_16x16x128_f8f6f4 v[46:49], v[2:9], v[216:223], 0, v197, v197 op_sel_hi:[0, 0, 0]
	v_mfma_scale_f32_16x16x128_f8f6f4 v[42:45], v[10:17], v[216:223], 0, v197, v197 op_sel_hi:[0, 0, 0]
	v_mfma_scale_f32_16x16x128_f8f6f4 v[38:41], v[2:9], v[224:231], 0, v197, v197 op_sel_hi:[0, 0, 0]
	v_mfma_scale_f32_16x16x128_f8f6f4 v[34:37], v[10:17], v[224:231], 0, v197, v197 op_sel_hi:[0, 0, 0]
	s_setprio 0
	s_barrier
; #define PG8_STAGE(bufoff, gbase, voff) do { _Pragma("unroll") for (int _i = 0; _i < 2; ++_i) \
;         __builtin_amdgcn_global_load_lds((const unsigned*)((const char*)(gbase) + (voff)[_i]), (PG8_LAS unsigned*)(lds + (bufoff) + ldsw + _i * 8192), 16, 0, 0); } while (0)
; #define PG8_LDA(dst, b, h) do { _Pragma("unroll") for (int m = 0; m < 4; ++m) Frag<F8>::load(dst[m], lds + PG8_SA(b, h) + aoff + m * 2048); } while (0)
; #define PG8_LDB(dst, b, h) do { _Pragma("unroll") for (int n = 0; n < 2; ++n) Frag<F8>::load(dst[n], lds + PG8_SB(b, h) + boff + n * 2048); } while (0)
; #define PG8_MMA(ai, bj, At, Bt) do { __builtin_amdgcn_s_setprio(3); _Pragma("unroll") for (int m = 0; m < 4; ++m) _Pragma("unroll") for (int n = 0; n < 2; ++n) Frag<F8>::mma(acc[ai][bj][m][n], Bt[n], At[m]); \
;         __builtin_amdgcn_s_setprio(0); } while (0)
; #define PG8_WAIT_V(n) asm volatile("s_waitcnt vmcnt(" #n ")" ::: "memory")
; #define PG8_WAIT_L(n) asm volatile("s_waitcnt lgkmcnt(" #n ")" ::: "memory")
; #define PG8_BAR __builtin_amdgcn_s_barrier()
; #define PG8_SCHED __builtin_amdgcn_sched_barrier(0)
; template <class Epi, class Sched, bool ALIGN_EPI = false, bool SP2 = false, bool F8 = false>
; __device__ __forceinline__ void gemm_phase(PG8_LAS unsigned char* lds, const Gemm g, const Sched& S, const Epi& E) {
;     ...
;             PG8_LDB(B0, 1, 0); PG8_LDB(B1, 1, 1); PG8_SCHED; PG8_LDA(At, 1, 0); PG8_STAGE(PG8_SA(0, 1), a2 + hstep, voffA);
;             PG8_WAIT_V(8); PG8_WAIT_L(0); PG8_BAR; PG8_MMA(0, 0, At, B0); PG8_MMA(0, 1, At, B1); PG8_BAR; PG8_SCHED;
;             PG8_LDA(At, 1, 1); PG8_STAGE(PG8_SB(1, 0), b3, voffB); PG8_STAGE(PG8_SB(1, 1), b3 + hstep, voffB); PG8_STAGE(PG8_SA(1, 0), a3, voffA);
;             PG8_WAIT_V(8); PG8_WAIT_L(0); PG8_BAR; PG8_MMA(1, 0, At, B0); PG8_MMA(1, 1, At, B1); PG8_BAR; PG8_SCHED;
	s_add_i32 s0, 0, 0x18000
	s_add_i32 s1, 0, 0x1c000
	v_add_u32_e32 v14, s0, v190
	v_add_u32_e32 v30, s1, v190
	ds_read_b128 v[2:5], v14
	ds_read_b128 v[6:9], v14 offset:1024
	ds_read_b128 v[10:13], v14 offset:2048
	ds_read_b128 v[14:17], v14 offset:3072
	ds_read_b128 v[18:21], v30
	ds_read_b128 v[22:25], v30 offset:1024
	ds_read_b128 v[26:29], v30 offset:2048
	ds_read_b128 v[30:33], v30 offset:3072
	s_add_u32 s4, s46, 0x20000
	s_addc_u32 s5, s47, 0
	s_mov_b32 m0, s72
	v_lshl_add_u64 v[232:233], s[4:5], 0, v[172:173]
	ds_read_b128 v[200:203], v196 offset:32768
	ds_read_b128 v[204:207], v196 offset:33792
	ds_read_b128 v[208:211], v196 offset:34816
	ds_read_b128 v[212:215], v196 offset:35840
	ds_read_b128 v[216:219], v196 offset:36864
	ds_read_b128 v[220:223], v196 offset:37888
	ds_read_b128 v[224:227], v196 offset:38912
	ds_read_b128 v[228:231], v196 offset:39936
	global_load_lds_dwordx4 v[232:233], off
	v_lshl_add_u64 v[232:233], s[4:5], 0, v[168:169]
	s_mov_b32 m0, s73
	s_nop 0
	global_load_lds_dwordx4 v[232:233], off
	s_waitcnt vmcnt(8)
	s_waitcnt lgkmcnt(0)
	s_barrier
	s_setprio 3
	s_waitcnt lgkmcnt(0)
	v_mfma_scale_f32_16x16x128_f8f6f4 v[158:161], v[2:9], v[200:207], v[158:161], v197, v197 op_sel_hi:[0,0,0]
	v_mfma_scale_f32_16x16x128_f8f6f4 v[154:157], v[10:17], v[200:207], v[154:157], v197, v197 op_sel_hi:[0,0,0]
	v_mfma_scale_f32_16x16x128_f8f6f4 v[150:153], v[2:9], v[208:215], v[150:153], v197, v197 op_sel_hi:[0,0,0]
	v_mfma_scale_f32_16x16x128_f8f6f4 v[142:145], v[10:17], v[208:215], v[142:145], v197, v197 op_sel_hi:[0,0,0]
	v_mfma_scale_f32_16x16x128_f8f6f4 v[130:133], v[2:9], v[216:223], v[130:133], v197, v197 op_sel_hi:[0,0,0]
	v_mfma_scale_f32_16x16x128_f8f6f4 v[122:125], v[10:17], v[216:223], v[122:125], v197, v197 op_sel_hi:[0,0,0]
	v_mfma_scale_f32_16x16x128_f8f6f4 v[118:121], v[2:9], v[224:231], v[118:121], v197, v197 op_sel_hi:[0,0,0]
	v_mfma_scale_f32_16x16x128_f8f6f4 v[110:113], v[10:17], v[224:231], v[110:113], v197, v197 op_sel_hi:[0,0,0]
	s_setprio 0
	s_setprio 3
	v_mfma_scale_f32_16x16x128_f8f6f4 v[146:149], v[18:25], v[200:207], v[146:149], v197, v197 op_sel_hi:[0,0,0]
	v_mfma_scale_f32_16x16x128_f8f6f4 v[138:141], v[26:33], v[200:207], v[138:141], v197, v197 op_sel_hi:[0,0,0]
	v_mfma_scale_f32_16x16x128_f8f6f4 v[134:137], v[18:25], v[208:215], v[134:137], v197, v197 op_sel_hi:[0,0,0]
	v_mfma_scale_f32_16x16x128_f8f6f4 v[126:129], v[26:33], v[208:215], v[126:129], v197, v197 op_sel_hi:[0,0,0]
	v_mfma_scale_f32_16x16x128_f8f6f4 v[114:117], v[18:25], v[216:223], v[114:117], v197, v197 op_sel_hi:[0,0,0]
	v_mfma_scale_f32_16x16x128_f8f6f4 v[106:109], v[26:33], v[216:223], v[106:109], v197, v197 op_sel_hi:[0,0,0]
	v_mfma_scale_f32_16x16x128_f8f6f4 v[102:105], v[18:25], v[224:231], v[102:105], v197, v197 op_sel_hi:[0,0,0]
	v_mfma_scale_f32_16x16x128_f8f6f4 v[98:101], v[26:33], v[224:231], v[98:101], v197, v197 op_sel_hi:[0,0,0]
	s_setprio 0
	s_barrier
	s_add_i32 s0, s0, s48
	v_lshl_add_u64 v[182:183], v[182:183], 0, s[18:19]
	s_mov_b32 m0, s0
	ds_read_b128 v[200:203], v196 offset:49152
	ds_read_b128 v[204:207], v196 offset:50176
	ds_read_b128 v[208:211], v196 offset:51200
	ds_read_b128 v[212:215], v196 offset:52224
	ds_read_b128 v[216:219], v196 offset:53248
	ds_read_b128 v[220:223], v196 offset:54272
	ds_read_b128 v[224:227], v196 offset:55296
	ds_read_b128 v[228:231], v196 offset:56320
	global_load_lds_dwordx4 v[182:183], off
	s_add_i32 m0, s0, 0x2000
	s_add_u32 s4, s44, 0x20080
	v_lshl_add_u64 v[182:183], v[184:185], 0, s[18:19]
	s_addc_u32 s5, s45, 0
	s_add_i32 s0, s1, s48
	global_load_lds_dwordx4 v[182:183], off
	v_lshl_add_u64 v[182:183], s[4:5], 0, v[170:171]
	s_mov_b32 m0, s0
	s_nop 0
	global_load_lds_dwordx4 v[182:183], off
	v_lshl_add_u64 v[182:183], s[4:5], 0, v[166:167]
	s_add_i32 m0, s0, 0x2000
	s_nop 0
	global_load_lds_dwordx4 v[182:183], off
	v_lshl_add_u64 v[182:183], v[186:187], 0, s[18:19]
	s_mov_b32 m0, s74
	s_nop 0
	global_load_lds_dwordx4 v[182:183], off
	v_lshl_add_u64 v[182:183], v[188:189], 0, s[18:19]
	s_mov_b32 m0, s75
	s_nop 0
	global_load_lds_dwordx4 v[182:183], off
	s_waitcnt vmcnt(8)
	s_waitcnt lgkmcnt(0)
	s_barrier
	s_setprio 3
	s_waitcnt lgkmcnt(0)
	v_mfma_scale_f32_16x16x128_f8f6f4 v[94:97], v[2:9], v[200:207], v[94:97], v197, v197 op_sel_hi:[0,0,0]
	v_mfma_scale_f32_16x16x128_f8f6f4 v[90:93], v[10:17], v[200:207], v[90:93], v197, v197 op_sel_hi:[0,0,0]
	v_mfma_scale_f32_16x16x128_f8f6f4 v[86:89], v[2:9], v[208:215], v[86:89], v197, v197 op_sel_hi:[0,0,0]
	v_mfma_scale_f32_16x16x128_f8f6f4 v[82:85], v[10:17], v[208:215], v[82:85], v197, v197 op_sel_hi:[0,0,0]
	v_mfma_scale_f32_16x16x128_f8f6f4 v[70:73], v[2:9], v[216:223], v[70:73], v197, v197 op_sel_hi:[0,0,0]
	v_mfma_scale_f32_16x16x128_f8f6f4 v[66:69], v[10:17], v[216:223], v[66:69], v197, v197 op_sel_hi:[0,0,0]
	v_mfma_scale_f32_16x16x128_f8f6f4 v[54:57], v[2:9], v[224:231], v[54:57], v197, v197 op_sel_hi:[0,0,0]
	v_mfma_scale_f32_16x16x128_f8f6f4 v[50:53], v[10:17], v[224:231], v[50:53], v197, v197 op_sel_hi:[0,0,0]
	s_setprio 0
	s_setprio 3
	v_mfma_scale_f32_16x16x128_f8f6f4 v[78:81], v[18:25], v[200:207], v[78:81], v197, v197 op_sel_hi:[0,0,0]
	v_mfma_scale_f32_16x16x128_f8f6f4 v[74:77], v[26:33], v[200:207], v[74:77], v197, v197 op_sel_hi:[0,0,0]
	v_mfma_scale_f32_16x16x128_f8f6f4 v[62:65], v[18:25], v[208:215], v[62:65], v197, v197 op_sel_hi:[0,0,0]
	v_mfma_scale_f32_16x16x128_f8f6f4 v[58:61], v[26:33], v[208:215], v[58:61], v197, v197 op_sel_hi:[0,0,0]
	v_mfma_scale_f32_16x16x128_f8f6f4 v[46:49], v[18:25], v[216:223], v[46:49], v197, v197 op_sel_hi:[0,0,0]
	v_mfma_scale_f32_16x16x128_f8f6f4 v[42:45], v[26:33], v[216:223], v[42:45], v197, v197 op_sel_hi:[0,0,0]
	v_mfma_scale_f32_16x16x128_f8f6f4 v[38:41], v[18:25], v[224:231], v[38:41], v197, v197 op_sel_hi:[0,0,0]
	v_mfma_scale_f32_16x16x128_f8f6f4 v[34:37], v[26:33], v[224:231], v[34:37], v197, v197 op_sel_hi:[0,0,0]
	s_setprio 0
	s_barrier
	s_add_i32 s87, s87, 2
	s_add_u32 s42, s42, 0x100
	s_addc_u32 s43, s43, 0
	s_add_u32 s85, s85, 0x100
	s_addc_u32 s86, s86, 0
	s_cmp_gt_u32 s87, 5
	s_cbranch_scc1 .Lpeel_exit_2

; #define PG8_STAGE(bufoff, gbase, voff) do { _Pragma("unroll") for (int _i = 0; _i < 2; ++_i) \
;         __builtin_amdgcn_global_load_lds((const unsigned*)((const char*)(gbase) + (voff)[_i]), (PG8_LAS unsigned*)(lds + (bufoff) + ldsw + _i * 8192), 16, 0, 0); } while (0)
; #define PG8_LDA(dst, b, h) do { _Pragma("unroll") for (int m = 0; m < 4; ++m) Frag<F8>::load(dst[m], lds + PG8_SA(b, h) + aoff + m * 2048); } while (0)
; #define PG8_LDB(dst, b, h) do { _Pragma("unroll") for (int n = 0; n < 2; ++n) Frag<F8>::load(dst[n], lds + PG8_SB(b, h) + boff + n * 2048); } while (0)
; #define PG8_MMA(ai, bj, At, Bt) do { __builtin_amdgcn_s_setprio(3); _Pragma("unroll") for (int m = 0; m < 4; ++m) _Pragma("unroll") for (int n = 0; n < 2; ++n) Frag<F8>::mma(acc[ai][bj][m][n], Bt[n], At[m]); \
;         __builtin_amdgcn_s_setprio(0); } while (0)
; #define PG8_WAIT_V(n) asm volatile("s_waitcnt vmcnt(" #n ")" ::: "memory")
; #define PG8_WAIT_L(n) asm volatile("s_waitcnt lgkmcnt(" #n ")" ::: "memory")
; #define PG8_BAR __builtin_amdgcn_s_barrier()
; #define PG8_SCHED __builtin_amdgcn_sched_barrier(0)
; template <class Epi, class Sched, bool ALIGN_EPI = false, bool SP2 = false, bool F8 = false>
; __device__ __forceinline__ void gemm_phase(PG8_LAS unsigned char* lds, const Gemm g, const Sched& S, const Epi& E) {
;     ...
;         for (int t = 0; t < nt; t += 2) {
;             const bool last = (t == nt - 2);
;             const char* a1 = cA + (size_t)(t + 1) * kstep;
;             const char* a2 = last ? nA : cA + (size_t)(t + 2) * kstep; const char* b2 = last ? nB : cB + (size_t)(t + 2) * kstep;
;             const char* a3 = a2 + kstep; const char* b3 = b2 + kstep;
;             if (last && has_next) S.a_ready(nxt);
;             if constexpr (SP2) {
;             PG8_LDB(B0, 0, 0); PG8_LDB(B1, 0, 1); PG8_SCHED; PG8_LDA(At, 0, 0); PG8_STAGE(PG8_SA(1, 1), a1 + hstep, voffA);
;             PG8_WAIT_V(8); PG8_WAIT_L(0); PG8_BAR; PG8_MMA(0, 0, At, B0); PG8_MMA(0, 1, At, B1); PG8_BAR; PG8_SCHED;
;             PG8_LDA(At, 0, 1); PG8_STAGE(PG8_SB(0, 0), b2, voffB); PG8_STAGE(PG8_SB(0, 1), b2 + hstep, voffB); PG8_STAGE(PG8_SA(0, 0), a2, voffA);
;             PG8_WAIT_V(8); PG8_WAIT_L(0); PG8_BAR; PG8_MMA(1, 0, At, B0); PG8_MMA(1, 1, At, B1); PG8_BAR; PG8_SCHED;
.LBB0_1309:
	s_ashr_i32 s25, s24, 31
	s_lshl_b64 s[4:5], s[24:25], 18
	s_add_u32 s30, s48, s4
	s_addc_u32 s31, s49, s5
	s_and_b64 s[4:5], s[22:23], exec
	s_cselect_b32 s25, s31, s43
	s_cselect_b32 s77, s30, s42
	s_ashr_i32 s27, s26, 31
	s_lshl_b64 s[4:5], s[26:27], 18
	s_add_u32 s36, s50, s4
	s_addc_u32 s37, s51, s5
	s_and_b64 s[4:5], s[22:23], exec
	s_cselect_b32 s27, s37, s45
	s_cselect_b32 s78, s36, s44
	s_add_u32 s42, s42, 0x20080
	s_addc_u32 s43, s43, 0
	s_add_u32 s79, s44, 0x100
	s_addc_u32 s80, s45, 0
	s_mov_b32 s81, -2
	ds_read_b128 v[18:21], v186
	ds_read_b128 v[22:25], v186 offset:1024
	ds_read_b128 v[26:29], v186 offset:2048
	ds_read_b128 v[30:33], v186 offset:3072
	ds_read_b128 v[2:5], v187
	ds_read_b128 v[6:9], v187 offset:1024
	ds_read_b128 v[10:13], v187 offset:2048
	ds_read_b128 v[14:17], v187 offset:3072
	s_add_u32 s0, s42, 0xfffe0080
	s_addc_u32 s1, s43, -1
	s_cmp_eq_u32 s81, 4
	s_cselect_b32 s47, s25, s1
	s_cselect_b32 s46, s77, s0
	s_cselect_b32 s45, s27, s80
	s_cselect_b32 s44, s78, s79
	v_lshl_add_u64 v[214:215], s[42:43], 0, v[172:173]
	s_add_i32 m0, s39, 0xc000
	ds_read_b128 v[176:179], v188
	ds_read_b128 v[180:183], v188 offset:1024
	ds_read_b128 v[190:193], v188 offset:2048
	ds_read_b128 v[194:197], v188 offset:3072
	ds_read_b128 v[198:201], v188 offset:4096
	ds_read_b128 v[202:205], v188 offset:5120
	ds_read_b128 v[206:209], v188 offset:6144
	ds_read_b128 v[210:213], v188 offset:7168
	global_load_lds_dwordx4 v[214:215], off
	v_lshl_add_u64 v[214:215], s[42:43], 0, v[174:175]
	s_add_i32 m0, s39, 0xe000
	s_nop 0
	global_load_lds_dwordx4 v[214:215], off
	s_waitcnt vmcnt(8)
	s_waitcnt lgkmcnt(0)
	s_barrier
	s_setprio 3
	s_waitcnt lgkmcnt(0)
	v_mfma_scale_f32_16x16x128_f8f6f4 v[158:161], v[18:25], v[176:183], 0, v189, v189 op_sel_hi:[0, 0, 0]
	v_mfma_scale_f32_16x16x128_f8f6f4 v[150:153], v[26:33], v[176:183], 0, v189, v189 op_sel_hi:[0, 0, 0]
	v_mfma_scale_f32_16x16x128_f8f6f4 v[142:145], v[18:25], v[190:197], 0, v189, v189 op_sel_hi:[0, 0, 0]
	v_mfma_scale_f32_16x16x128_f8f6f4 v[134:137], v[26:33], v[190:197], 0, v189, v189 op_sel_hi:[0, 0, 0]
	v_mfma_scale_f32_16x16x128_f8f6f4 v[126:129], v[18:25], v[198:205], 0, v189, v189 op_sel_hi:[0, 0, 0]
	v_mfma_scale_f32_16x16x128_f8f6f4 v[118:121], v[26:33], v[198:205], 0, v189, v189 op_sel_hi:[0, 0, 0]
	v_mfma_scale_f32_16x16x128_f8f6f4 v[110:113], v[18:25], v[206:213], 0, v189, v189 op_sel_hi:[0, 0, 0]
	v_mfma_scale_f32_16x16x128_f8f6f4 v[102:105], v[26:33], v[206:213], 0, v189, v189 op_sel_hi:[0, 0, 0]
	s_setprio 0
	s_setprio 3
	v_mfma_scale_f32_16x16x128_f8f6f4 v[154:157], v[2:9], v[176:183], 0, v189, v189 op_sel_hi:[0, 0, 0]
	v_mfma_scale_f32_16x16x128_f8f6f4 v[146:149], v[10:17], v[176:183], 0, v189, v189 op_sel_hi:[0, 0, 0]
	v_mfma_scale_f32_16x16x128_f8f6f4 v[138:141], v[2:9], v[190:197], 0, v189, v189 op_sel_hi:[0, 0, 0]
	v_mfma_scale_f32_16x16x128_f8f6f4 v[130:133], v[10:17], v[190:197], 0, v189, v189 op_sel_hi:[0, 0, 0]
	v_mfma_scale_f32_16x16x128_f8f6f4 v[122:125], v[2:9], v[198:205], 0, v189, v189 op_sel_hi:[0, 0, 0]
	v_mfma_scale_f32_16x16x128_f8f6f4 v[114:117], v[10:17], v[198:205], 0, v189, v189 op_sel_hi:[0, 0, 0]
	v_mfma_scale_f32_16x16x128_f8f6f4 v[106:109], v[2:9], v[206:213], 0, v189, v189 op_sel_hi:[0, 0, 0]
	v_mfma_scale_f32_16x16x128_f8f6f4 v[98:101], v[10:17], v[206:213], 0, v189, v189 op_sel_hi:[0, 0, 0]
	s_setprio 0
	s_barrier
	s_add_i32 s0, s74, s52
	v_lshl_add_u64 v[176:177], s[44:45], 0, v[168:169]
	s_mov_b32 m0, s0
	ds_read_b128 v[190:193], v188 offset:16384
	ds_read_b128 v[194:197], v188 offset:17408
	ds_read_b128 v[198:201], v188 offset:18432
	ds_read_b128 v[202:205], v188 offset:19456
	ds_read_b128 v[206:209], v188 offset:20480
	ds_read_b128 v[210:213], v188 offset:21504
	ds_read_b128 v[214:217], v188 offset:22528
	ds_read_b128 v[218:221], v188 offset:23552
	global_load_lds_dwordx4 v[176:177], off
	s_add_i32 m0, s0, 0x2000
	s_add_u32 s4, s44, 0x20000
	v_lshl_add_u64 v[178:179], s[44:45], 0, v[164:165]
	s_addc_u32 s5, s45, 0
	s_add_i32 s0, s75, s52
	global_load_lds_dwordx4 v[178:179], off
	v_lshl_add_u64 v[180:181], s[4:5], 0, v[168:169]
	s_mov_b32 m0, s0
	v_lshl_add_u64 v[182:183], s[46:47], 0, v[166:167]
	global_load_lds_dwordx4 v[180:181], off
	v_lshl_add_u64 v[180:181], s[4:5], 0, v[164:165]
	s_add_i32 m0, s0, 0x2000
	s_nop 0
	global_load_lds_dwordx4 v[180:181], off
	v_lshl_add_u64 v[180:181], s[46:47], 0, v[170:171]
	s_mov_b32 m0, s39
	s_nop 0
	global_load_lds_dwordx4 v[180:181], off
	s_mov_b32 m0, s41
	s_nop 0
	global_load_lds_dwordx4 v[182:183], off
	s_waitcnt vmcnt(8)
	s_waitcnt lgkmcnt(0)
	s_barrier
	s_setprio 3
	s_waitcnt lgkmcnt(0)
	v_mfma_scale_f32_16x16x128_f8f6f4 v[94:97], v[18:25], v[190:197], 0, v189, v189 op_sel_hi:[0, 0, 0]
	v_mfma_scale_f32_16x16x128_f8f6f4 v[86:89], v[26:33], v[190:197], 0, v189, v189 op_sel_hi:[0, 0, 0]
	v_mfma_scale_f32_16x16x128_f8f6f4 v[78:81], v[18:25], v[198:205], 0, v189, v189 op_sel_hi:[0, 0, 0]
	v_mfma_scale_f32_16x16x128_f8f6f4 v[70:73], v[26:33], v[198:205], 0, v189, v189 op_sel_hi:[0, 0, 0]
	v_mfma_scale_f32_16x16x128_f8f6f4 v[62:65], v[18:25], v[206:213], 0, v189, v189 op_sel_hi:[0, 0, 0]
	v_mfma_scale_f32_16x16x128_f8f6f4 v[54:57], v[26:33], v[206:213], 0, v189, v189 op_sel_hi:[0, 0, 0]
	v_mfma_scale_f32_16x16x128_f8f6f4 v[46:49], v[18:25], v[214:221], 0, v189, v189 op_sel_hi:[0, 0, 0]
	v_mfma_scale_f32_16x16x128_f8f6f4 v[38:41], v[26:33], v[214:221], 0, v189, v189 op_sel_hi:[0, 0, 0]
	s_setprio 0
	s_setprio 3
	v_mfma_scale_f32_16x16x128_f8f6f4 v[90:93], v[2:9], v[190:197], 0, v189, v189 op_sel_hi:[0, 0, 0]
	v_mfma_scale_f32_16x16x128_f8f6f4 v[82:85], v[10:17], v[190:197], 0, v189, v189 op_sel_hi:[0, 0, 0]
	v_mfma_scale_f32_16x16x128_f8f6f4 v[74:77], v[2:9], v[198:205], 0, v189, v189 op_sel_hi:[0, 0, 0]
	v_mfma_scale_f32_16x16x128_f8f6f4 v[66:69], v[10:17], v[198:205], 0, v189, v189 op_sel_hi:[0, 0, 0]
	v_mfma_scale_f32_16x16x128_f8f6f4 v[58:61], v[2:9], v[206:213], 0, v189, v189 op_sel_hi:[0, 0, 0]
	v_mfma_scale_f32_16x16x128_f8f6f4 v[50:53], v[10:17], v[206:213], 0, v189, v189 op_sel_hi:[0, 0, 0]
	v_mfma_scale_f32_16x16x128_f8f6f4 v[42:45], v[2:9], v[214:221], 0, v189, v189 op_sel_hi:[0, 0, 0]
	v_mfma_scale_f32_16x16x128_f8f6f4 v[34:37], v[10:17], v[214:221], 0, v189, v189 op_sel_hi:[0, 0, 0]
	s_setprio 0
	s_barrier
; #define PG8_STAGE(bufoff, gbase, voff) do { _Pragma("unroll") for (int _i = 0; _i < 2; ++_i) \
;         __builtin_amdgcn_global_load_lds((const unsigned*)((const char*)(gbase) + (voff)[_i]), (PG8_LAS unsigned*)(lds + (bufoff) + ldsw + _i * 8192), 16, 0, 0); } while (0)
; #define PG8_LDA(dst, b, h) do { _Pragma("unroll") for (int m = 0; m < 4; ++m) Frag<F8>::load(dst[m], lds + PG8_SA(b, h) + aoff + m * 2048); } while (0)
; #define PG8_LDB(dst, b, h) do { _Pragma("unroll") for (int n = 0; n < 2; ++n) Frag<F8>::load(dst[n], lds + PG8_SB(b, h) + boff + n * 2048); } while (0)
; #define PG8_MMA(ai, bj, At, Bt) do { __builtin_amdgcn_s_setprio(3); _Pragma("unroll") for (int m = 0; m < 4; ++m) _Pragma("unroll") for (int n = 0; n < 2; ++n) Frag<F8>::mma(acc[ai][bj][m][n], Bt[n], At[m]); \
;         __builtin_amdgcn_s_setprio(0); } while (0)
; #define PG8_WAIT_V(n) asm volatile("s_waitcnt vmcnt(" #n ")" ::: "memory")
; #define PG8_WAIT_L(n) asm volatile("s_waitcnt lgkmcnt(" #n ")" ::: "memory")
; #define PG8_BAR __builtin_amdgcn_s_barrier()
; #define PG8_SCHED __builtin_amdgcn_sched_barrier(0)
; template <class Epi, class Sched, bool ALIGN_EPI = false, bool SP2 = false, bool F8 = false>
; __device__ __forceinline__ void gemm_phase(PG8_LAS unsigned char* lds, const Gemm g, const Sched& S, const Epi& E) {
;     ...
;             PG8_LDB(B0, 1, 0); PG8_LDB(B1, 1, 1); PG8_SCHED; PG8_LDA(At, 1, 0); PG8_STAGE(PG8_SA(0, 1), a2 + hstep, voffA);
;             PG8_WAIT_V(8); PG8_WAIT_L(0); PG8_BAR; PG8_MMA(0, 0, At, B0); PG8_MMA(0, 1, At, B1); PG8_BAR; PG8_SCHED;
;             PG8_LDA(At, 1, 1); PG8_STAGE(PG8_SB(1, 0), b3, voffB); PG8_STAGE(PG8_SB(1, 1), b3 + hstep, voffB); PG8_STAGE(PG8_SA(1, 0), a3, voffA);
;             PG8_WAIT_V(8); PG8_WAIT_L(0); PG8_BAR; PG8_MMA(1, 0, At, B0); PG8_MMA(1, 1, At, B1); PG8_BAR; PG8_SCHED;
	s_add_i32 s0, 0, 0x18000
	s_add_i32 s1, 0, 0x1c000
	v_add_u32_e32 v14, s0, v184
	v_add_u32_e32 v30, s1, v184
	ds_read_b128 v[2:5], v14
	ds_read_b128 v[6:9], v14 offset:1024
	ds_read_b128 v[10:13], v14 offset:2048
	ds_read_b128 v[14:17], v14 offset:3072
	ds_read_b128 v[18:21], v30
	ds_read_b128 v[22:25], v30 offset:1024
	ds_read_b128 v[26:29], v30 offset:2048
	ds_read_b128 v[30:33], v30 offset:3072
	s_add_u32 s4, s46, 0x20000
	s_addc_u32 s5, s47, 0
	s_mov_b32 m0, s58
	v_lshl_add_u64 v[222:223], s[4:5], 0, v[170:171]
	ds_read_b128 v[190:193], v188 offset:32768
	ds_read_b128 v[194:197], v188 offset:33792
	ds_read_b128 v[198:201], v188 offset:34816
	ds_read_b128 v[202:205], v188 offset:35840
	ds_read_b128 v[206:209], v188 offset:36864
	ds_read_b128 v[210:213], v188 offset:37888
	ds_read_b128 v[214:217], v188 offset:38912
	ds_read_b128 v[218:221], v188 offset:39936
	global_load_lds_dwordx4 v[222:223], off
	v_lshl_add_u64 v[222:223], s[4:5], 0, v[166:167]
	s_mov_b32 m0, s59
	s_nop 0
	global_load_lds_dwordx4 v[222:223], off
	s_waitcnt vmcnt(8)
	s_waitcnt lgkmcnt(0)
	s_barrier
	s_setprio 3
	s_waitcnt lgkmcnt(0)
	v_mfma_scale_f32_16x16x128_f8f6f4 v[158:161], v[2:9], v[190:197], v[158:161], v189, v189 op_sel_hi:[0,0,0]
	v_mfma_scale_f32_16x16x128_f8f6f4 v[150:153], v[10:17], v[190:197], v[150:153], v189, v189 op_sel_hi:[0,0,0]
	v_mfma_scale_f32_16x16x128_f8f6f4 v[142:145], v[2:9], v[198:205], v[142:145], v189, v189 op_sel_hi:[0,0,0]
	v_mfma_scale_f32_16x16x128_f8f6f4 v[134:137], v[10:17], v[198:205], v[134:137], v189, v189 op_sel_hi:[0,0,0]
	v_mfma_scale_f32_16x16x128_f8f6f4 v[126:129], v[2:9], v[206:213], v[126:129], v189, v189 op_sel_hi:[0,0,0]
	v_mfma_scale_f32_16x16x128_f8f6f4 v[118:121], v[10:17], v[206:213], v[118:121], v189, v189 op_sel_hi:[0,0,0]
	v_mfma_scale_f32_16x16x128_f8f6f4 v[110:113], v[2:9], v[214:221], v[110:113], v189, v189 op_sel_hi:[0,0,0]
	v_mfma_scale_f32_16x16x128_f8f6f4 v[102:105], v[10:17], v[214:221], v[102:105], v189, v189 op_sel_hi:[0,0,0]
	s_setprio 0
	s_setprio 3
	v_mfma_scale_f32_16x16x128_f8f6f4 v[154:157], v[18:25], v[190:197], v[154:157], v189, v189 op_sel_hi:[0,0,0]
	v_mfma_scale_f32_16x16x128_f8f6f4 v[146:149], v[26:33], v[190:197], v[146:149], v189, v189 op_sel_hi:[0,0,0]
	v_mfma_scale_f32_16x16x128_f8f6f4 v[138:141], v[18:25], v[198:205], v[138:141], v189, v189 op_sel_hi:[0,0,0]
	v_mfma_scale_f32_16x16x128_f8f6f4 v[130:133], v[26:33], v[198:205], v[130:133], v189, v189 op_sel_hi:[0,0,0]
	v_mfma_scale_f32_16x16x128_f8f6f4 v[122:125], v[18:25], v[206:213], v[122:125], v189, v189 op_sel_hi:[0,0,0]
	v_mfma_scale_f32_16x16x128_f8f6f4 v[114:117], v[26:33], v[206:213], v[114:117], v189, v189 op_sel_hi:[0,0,0]
	v_mfma_scale_f32_16x16x128_f8f6f4 v[106:109], v[18:25], v[214:221], v[106:109], v189, v189 op_sel_hi:[0,0,0]
	v_mfma_scale_f32_16x16x128_f8f6f4 v[98:101], v[26:33], v[214:221], v[98:101], v189, v189 op_sel_hi:[0,0,0]
	s_setprio 0
	s_barrier
	s_add_i32 s0, s0, s52
	v_lshl_add_u64 v[176:177], v[176:177], 0, s[14:15]
	s_mov_b32 m0, s0
	ds_read_b128 v[190:193], v188 offset:49152
	ds_read_b128 v[194:197], v188 offset:50176
	ds_read_b128 v[198:201], v188 offset:51200
	ds_read_b128 v[202:205], v188 offset:52224
	ds_read_b128 v[206:209], v188 offset:53248
	ds_read_b128 v[210:213], v188 offset:54272
	ds_read_b128 v[214:217], v188 offset:55296
	ds_read_b128 v[218:221], v188 offset:56320
	global_load_lds_dwordx4 v[176:177], off
	s_add_i32 m0, s0, 0x2000
	s_add_u32 s4, s44, 0x20080
	v_lshl_add_u64 v[176:177], v[178:179], 0, s[14:15]
	s_addc_u32 s5, s45, 0
	s_add_i32 s0, s1, s52
	global_load_lds_dwordx4 v[176:177], off
	v_lshl_add_u64 v[176:177], s[4:5], 0, v[168:169]
	s_mov_b32 m0, s0
	s_nop 0
	global_load_lds_dwordx4 v[176:177], off
	v_lshl_add_u64 v[176:177], s[4:5], 0, v[164:165]
	s_add_i32 m0, s0, 0x2000
	s_nop 0
	global_load_lds_dwordx4 v[176:177], off
	v_lshl_add_u64 v[176:177], v[180:181], 0, s[14:15]
	s_mov_b32 m0, s60
	s_nop 0
	global_load_lds_dwordx4 v[176:177], off
	v_lshl_add_u64 v[176:177], v[182:183], 0, s[14:15]
	s_mov_b32 m0, s61
	s_nop 0
	global_load_lds_dwordx4 v[176:177], off
	s_waitcnt vmcnt(8)
	s_waitcnt lgkmcnt(0)
	s_barrier
	s_setprio 3
	s_waitcnt lgkmcnt(0)
	v_mfma_scale_f32_16x16x128_f8f6f4 v[94:97], v[2:9], v[190:197], v[94:97], v189, v189 op_sel_hi:[0,0,0]
	v_mfma_scale_f32_16x16x128_f8f6f4 v[86:89], v[10:17], v[190:197], v[86:89], v189, v189 op_sel_hi:[0,0,0]
	v_mfma_scale_f32_16x16x128_f8f6f4 v[78:81], v[2:9], v[198:205], v[78:81], v189, v189 op_sel_hi:[0,0,0]
	v_mfma_scale_f32_16x16x128_f8f6f4 v[70:73], v[10:17], v[198:205], v[70:73], v189, v189 op_sel_hi:[0,0,0]
	v_mfma_scale_f32_16x16x128_f8f6f4 v[62:65], v[2:9], v[206:213], v[62:65], v189, v189 op_sel_hi:[0,0,0]
	v_mfma_scale_f32_16x16x128_f8f6f4 v[54:57], v[10:17], v[206:213], v[54:57], v189, v189 op_sel_hi:[0,0,0]
	v_mfma_scale_f32_16x16x128_f8f6f4 v[46:49], v[2:9], v[214:221], v[46:49], v189, v189 op_sel_hi:[0,0,0]
	v_mfma_scale_f32_16x16x128_f8f6f4 v[38:41], v[10:17], v[214:221], v[38:41], v189, v189 op_sel_hi:[0,0,0]
	s_setprio 0
	s_setprio 3
	v_mfma_scale_f32_16x16x128_f8f6f4 v[90:93], v[18:25], v[190:197], v[90:93], v189, v189 op_sel_hi:[0,0,0]
	v_mfma_scale_f32_16x16x128_f8f6f4 v[82:85], v[26:33], v[190:197], v[82:85], v189, v189 op_sel_hi:[0,0,0]
	v_mfma_scale_f32_16x16x128_f8f6f4 v[74:77], v[18:25], v[198:205], v[74:77], v189, v189 op_sel_hi:[0,0,0]
	v_mfma_scale_f32_16x16x128_f8f6f4 v[66:69], v[26:33], v[198:205], v[66:69], v189, v189 op_sel_hi:[0,0,0]
	v_mfma_scale_f32_16x16x128_f8f6f4 v[58:61], v[18:25], v[206:213], v[58:61], v189, v189 op_sel_hi:[0,0,0]
	v_mfma_scale_f32_16x16x128_f8f6f4 v[50:53], v[26:33], v[206:213], v[50:53], v189, v189 op_sel_hi:[0,0,0]
	v_mfma_scale_f32_16x16x128_f8f6f4 v[42:45], v[18:25], v[214:221], v[42:45], v189, v189 op_sel_hi:[0,0,0]
	v_mfma_scale_f32_16x16x128_f8f6f4 v[34:37], v[26:33], v[214:221], v[34:37], v189, v189 op_sel_hi:[0,0,0]
	s_setprio 0
	s_barrier
	s_add_i32 s81, s81, 2
	s_add_u32 s42, s42, 0x100
	s_addc_u32 s43, s43, 0
	s_add_u32 s79, s79, 0x100
	s_addc_u32 s80, s80, 0
	s_cmp_gt_u32 s81, 5
	s_cbranch_scc1 .Lpeel_exit_3

; #define PG8_BAR __builtin_amdgcn_s_barrier()
; #define PG8_SCHED __builtin_amdgcn_sched_barrier(0)
; template <class Epi, class Sched, bool ALIGN_EPI = false, bool SP2 = false, bool F8 = false>
; __device__ __forceinline__ void gemm_phase(PG8_LAS unsigned char* lds, const Gemm g, const Sched& S, const Epi& E) {
;     ...
;         }
;         if constexpr (ALIGN_EPI) { if (wr == 0) PG8_BAR; }
;         if constexpr (F8) { asm volatile("s_nop 15\n\ts_nop 15" ::: "memory"); PG8_SCHED; }
;         if constexpr (!Epi::AFTER_DRAIN) { E(acc, cur, wr, wc, fr, fq); S.done(cur); }
.Lpeel_exit_3:
	s_and_b64 vcc, exec, s[16:17]
	s_cbranch_vccz .LBB0_1313
	s_barrier

; #define PG8_STAGE(bufoff, gbase, voff) do { _Pragma("unroll") for (int _i = 0; _i < 2; ++_i) \
;         __builtin_amdgcn_global_load_lds((const unsigned*)((const char*)(gbase) + (voff)[_i]), (PG8_LAS unsigned*)(lds + (bufoff) + ldsw + _i * 8192), 16, 0, 0); } while (0)
; #define PG8_LDA(dst, b, h) do { _Pragma("unroll") for (int m = 0; m < 4; ++m) Frag<F8>::load(dst[m], lds + PG8_SA(b, h) + aoff + m * 2048); } while (0)
; #define PG8_LDB(dst, b, h) do { _Pragma("unroll") for (int n = 0; n < 2; ++n) Frag<F8>::load(dst[n], lds + PG8_SB(b, h) + boff + n * 2048); } while (0)
; #define PG8_MMA(ai, bj, At, Bt) do { __builtin_amdgcn_s_setprio(3); _Pragma("unroll") for (int m = 0; m < 4; ++m) _Pragma("unroll") for (int n = 0; n < 2; ++n) Frag<F8>::mma(acc[ai][bj][m][n], Bt[n], At[m]); \
;         __builtin_amdgcn_s_setprio(0); } while (0)
; #define PG8_WAIT_V(n) asm volatile("s_waitcnt vmcnt(" #n ")" ::: "memory")
; #define PG8_WAIT_L(n) asm volatile("s_waitcnt lgkmcnt(" #n ")" ::: "memory")
; #define PG8_BAR __builtin_amdgcn_s_barrier()
; #define PG8_SCHED __builtin_amdgcn_sched_barrier(0)
; template <class Epi, class Sched, bool ALIGN_EPI = false, bool SP2 = false, bool F8 = false>
; __device__ __forceinline__ void gemm_phase(PG8_LAS unsigned char* lds, const Gemm g, const Sched& S, const Epi& E) {
;     ...
;         for (int t = 0; t < nt; t += 2) {
;             const bool last = (t == nt - 2);
;             const char* a1 = cA + (size_t)(t + 1) * kstep;
;             const char* a2 = last ? nA : cA + (size_t)(t + 2) * kstep; const char* b2 = last ? nB : cB + (size_t)(t + 2) * kstep;
;             const char* a3 = a2 + kstep; const char* b3 = b2 + kstep;
;             if (last && has_next) S.a_ready(nxt);
;             if constexpr (SP2) {
;             PG8_LDB(B0, 0, 0); PG8_LDB(B1, 0, 1); PG8_SCHED; PG8_LDA(At, 0, 0); PG8_STAGE(PG8_SA(1, 1), a1 + hstep, voffA);
;             PG8_WAIT_V(8); PG8_WAIT_L(0); PG8_BAR; PG8_MMA(0, 0, At, B0); PG8_MMA(0, 1, At, B1); PG8_BAR; PG8_SCHED;
;             PG8_LDA(At, 0, 1); PG8_STAGE(PG8_SB(0, 0), b2, voffB); PG8_STAGE(PG8_SB(0, 1), b2 + hstep, voffB); PG8_STAGE(PG8_SA(0, 0), a2, voffA);
;             PG8_WAIT_V(8); PG8_WAIT_L(0); PG8_BAR; PG8_MMA(1, 0, At, B0); PG8_MMA(1, 1, At, B1); PG8_BAR; PG8_SCHED;
.LBB0_1391:
	v_lshl_add_u64 v[180:181], v[2:3], 0, s[24:25]
	s_mov_b32 s76, -2
	ds_read_b128 v[18:21], v192
	ds_read_b128 v[22:25], v192 offset:1024
	ds_read_b128 v[26:29], v192 offset:2048
	ds_read_b128 v[30:33], v192 offset:3072
	ds_read_b128 v[2:5], v193
	ds_read_b128 v[6:9], v193 offset:1024
	ds_read_b128 v[10:13], v193 offset:2048
	ds_read_b128 v[14:17], v193 offset:3072
	s_add_u32 s30, s36, 0x100
	s_addc_u32 s31, s37, 0
	s_cmp_eq_u32 s76, 24
	s_cselect_b64 vcc, -1, 0
	s_cselect_b32 s39, s27, s31
	s_cselect_b32 s38, s26, s30
	v_cndmask_b32_e32 v183, v181, v179, vcc
	v_cndmask_b32_e32 v182, v180, v178, vcc
	s_mov_b32 m0, s56
	v_lshl_add_u64 v[224:225], s[36:37], 0, v[174:175]
	ds_read_b128 v[184:187], v194
	ds_read_b128 v[188:191], v194 offset:1024
	ds_read_b128 v[200:203], v194 offset:2048
	ds_read_b128 v[204:207], v194 offset:3072
	ds_read_b128 v[208:211], v194 offset:4096
	ds_read_b128 v[212:215], v194 offset:5120
	ds_read_b128 v[216:219], v194 offset:6144
	ds_read_b128 v[220:223], v194 offset:7168
	global_load_lds_dwordx4 v[224:225], off
	v_lshl_add_u64 v[224:225], s[36:37], 0, v[176:177]
	s_mov_b32 m0, s57
	s_nop 0
	global_load_lds_dwordx4 v[224:225], off
	s_waitcnt vmcnt(8)
	s_waitcnt lgkmcnt(0)
	s_barrier
	s_setprio 3
	s_waitcnt lgkmcnt(0)
	v_mfma_scale_f32_16x16x128_f8f6f4 v[158:161], v[18:25], v[184:191], 0, v195, v195 op_sel_hi:[0, 0, 0]
	v_mfma_scale_f32_16x16x128_f8f6f4 v[154:157], v[26:33], v[184:191], 0, v195, v195 op_sel_hi:[0, 0, 0]
	v_mfma_scale_f32_16x16x128_f8f6f4 v[142:145], v[18:25], v[200:207], 0, v195, v195 op_sel_hi:[0, 0, 0]
	v_mfma_scale_f32_16x16x128_f8f6f4 v[138:141], v[26:33], v[200:207], 0, v195, v195 op_sel_hi:[0, 0, 0]
	v_mfma_scale_f32_16x16x128_f8f6f4 v[126:129], v[18:25], v[208:215], 0, v195, v195 op_sel_hi:[0, 0, 0]
	v_mfma_scale_f32_16x16x128_f8f6f4 v[122:125], v[26:33], v[208:215], 0, v195, v195 op_sel_hi:[0, 0, 0]
	v_mfma_scale_f32_16x16x128_f8f6f4 v[110:113], v[18:25], v[216:223], 0, v195, v195 op_sel_hi:[0, 0, 0]
	v_mfma_scale_f32_16x16x128_f8f6f4 v[106:109], v[26:33], v[216:223], 0, v195, v195 op_sel_hi:[0, 0, 0]
	s_setprio 0
	s_setprio 3
	v_mfma_scale_f32_16x16x128_f8f6f4 v[150:153], v[2:9], v[184:191], 0, v195, v195 op_sel_hi:[0, 0, 0]
	v_mfma_scale_f32_16x16x128_f8f6f4 v[146:149], v[10:17], v[184:191], 0, v195, v195 op_sel_hi:[0, 0, 0]
	v_mfma_scale_f32_16x16x128_f8f6f4 v[134:137], v[2:9], v[200:207], 0, v195, v195 op_sel_hi:[0, 0, 0]
	v_mfma_scale_f32_16x16x128_f8f6f4 v[130:133], v[10:17], v[200:207], 0, v195, v195 op_sel_hi:[0, 0, 0]
	v_mfma_scale_f32_16x16x128_f8f6f4 v[118:121], v[2:9], v[208:215], 0, v195, v195 op_sel_hi:[0, 0, 0]
	v_mfma_scale_f32_16x16x128_f8f6f4 v[114:117], v[10:17], v[208:215], 0, v195, v195 op_sel_hi:[0, 0, 0]
	v_mfma_scale_f32_16x16x128_f8f6f4 v[102:105], v[2:9], v[216:223], 0, v195, v195 op_sel_hi:[0, 0, 0]
	v_mfma_scale_f32_16x16x128_f8f6f4 v[98:101], v[10:17], v[216:223], 0, v195, v195 op_sel_hi:[0, 0, 0]
	s_setprio 0
	s_barrier
	s_mov_b32 m0, s58
	v_lshl_add_u64 v[184:185], v[182:183], 0, v[166:167]
	ds_read_b128 v[200:203], v194 offset:16384
	ds_read_b128 v[204:207], v194 offset:17408
	ds_read_b128 v[208:211], v194 offset:18432
	ds_read_b128 v[212:215], v194 offset:19456
	ds_read_b128 v[216:219], v194 offset:20480
	ds_read_b128 v[220:223], v194 offset:21504
	ds_read_b128 v[224:227], v194 offset:22528
	ds_read_b128 v[228:231], v194 offset:23552
	global_load_lds_dwordx4 v[184:185], off
	v_lshl_add_u64 v[186:187], v[182:183], 0, v[170:171]
	s_mov_b32 m0, s59
	v_lshl_add_u64 v[188:189], v[182:183], 0, s[10:11]
	global_load_lds_dwordx4 v[186:187], off
	v_lshl_add_u64 v[190:191], v[188:189], 0, v[166:167]
	s_mov_b32 m0, s60
	v_lshl_add_u64 v[188:189], v[188:189], 0, v[170:171]
	global_load_lds_dwordx4 v[190:191], off
	s_mov_b32 m0, s61
	v_lshl_add_u64 v[190:191], s[38:39], 0, v[168:169]
	global_load_lds_dwordx4 v[188:189], off
	v_lshl_add_u64 v[188:189], s[38:39], 0, v[164:165]
	s_mov_b32 m0, s45
	s_nop 0
	global_load_lds_dwordx4 v[188:189], off
	s_mov_b32 m0, s46
	s_nop 0
	global_load_lds_dwordx4 v[190:191], off
	s_waitcnt vmcnt(8)
	s_waitcnt lgkmcnt(0)
	s_barrier
	s_setprio 3
	s_waitcnt lgkmcnt(0)
	v_mfma_scale_f32_16x16x128_f8f6f4 v[94:97], v[18:25], v[200:207], 0, v195, v195 op_sel_hi:[0, 0, 0]
	v_mfma_scale_f32_16x16x128_f8f6f4 v[90:93], v[26:33], v[200:207], 0, v195, v195 op_sel_hi:[0, 0, 0]
	v_mfma_scale_f32_16x16x128_f8f6f4 v[78:81], v[18:25], v[208:215], 0, v195, v195 op_sel_hi:[0, 0, 0]
	v_mfma_scale_f32_16x16x128_f8f6f4 v[74:77], v[26:33], v[208:215], 0, v195, v195 op_sel_hi:[0, 0, 0]
	v_mfma_scale_f32_16x16x128_f8f6f4 v[62:65], v[18:25], v[216:223], 0, v195, v195 op_sel_hi:[0, 0, 0]
	v_mfma_scale_f32_16x16x128_f8f6f4 v[58:61], v[26:33], v[216:223], 0, v195, v195 op_sel_hi:[0, 0, 0]
	v_mfma_scale_f32_16x16x128_f8f6f4 v[46:49], v[18:25], v[224:231], 0, v195, v195 op_sel_hi:[0, 0, 0]
	v_mfma_scale_f32_16x16x128_f8f6f4 v[42:45], v[26:33], v[224:231], 0, v195, v195 op_sel_hi:[0, 0, 0]
	s_setprio 0
	s_setprio 3
	v_mfma_scale_f32_16x16x128_f8f6f4 v[86:89], v[2:9], v[200:207], 0, v195, v195 op_sel_hi:[0, 0, 0]
	v_mfma_scale_f32_16x16x128_f8f6f4 v[82:85], v[10:17], v[200:207], 0, v195, v195 op_sel_hi:[0, 0, 0]
	v_mfma_scale_f32_16x16x128_f8f6f4 v[70:73], v[2:9], v[208:215], 0, v195, v195 op_sel_hi:[0, 0, 0]
	v_mfma_scale_f32_16x16x128_f8f6f4 v[66:69], v[10:17], v[208:215], 0, v195, v195 op_sel_hi:[0, 0, 0]
	v_mfma_scale_f32_16x16x128_f8f6f4 v[54:57], v[2:9], v[216:223], 0, v195, v195 op_sel_hi:[0, 0, 0]
	v_mfma_scale_f32_16x16x128_f8f6f4 v[50:53], v[10:17], v[216:223], 0, v195, v195 op_sel_hi:[0, 0, 0]
	v_mfma_scale_f32_16x16x128_f8f6f4 v[38:41], v[2:9], v[224:231], 0, v195, v195 op_sel_hi:[0, 0, 0]
	v_mfma_scale_f32_16x16x128_f8f6f4 v[34:37], v[10:17], v[224:231], 0, v195, v195 op_sel_hi:[0, 0, 0]
	s_setprio 0
	s_barrier
; #define PG8_STAGE(bufoff, gbase, voff) do { _Pragma("unroll") for (int _i = 0; _i < 2; ++_i) \
;         __builtin_amdgcn_global_load_lds((const unsigned*)((const char*)(gbase) + (voff)[_i]), (PG8_LAS unsigned*)(lds + (bufoff) + ldsw + _i * 8192), 16, 0, 0); } while (0)
; #define PG8_LDA(dst, b, h) do { _Pragma("unroll") for (int m = 0; m < 4; ++m) Frag<F8>::load(dst[m], lds + PG8_SA(b, h) + aoff + m * 2048); } while (0)
; #define PG8_LDB(dst, b, h) do { _Pragma("unroll") for (int n = 0; n < 2; ++n) Frag<F8>::load(dst[n], lds + PG8_SB(b, h) + boff + n * 2048); } while (0)
; #define PG8_MMA(ai, bj, At, Bt) do { __builtin_amdgcn_s_setprio(3); _Pragma("unroll") for (int m = 0; m < 4; ++m) _Pragma("unroll") for (int n = 0; n < 2; ++n) Frag<F8>::mma(acc[ai][bj][m][n], Bt[n], At[m]); \
;         __builtin_amdgcn_s_setprio(0); } while (0)
; #define PG8_WAIT_V(n) asm volatile("s_waitcnt vmcnt(" #n ")" ::: "memory")
; #define PG8_WAIT_L(n) asm volatile("s_waitcnt lgkmcnt(" #n ")" ::: "memory")
; #define PG8_BAR __builtin_amdgcn_s_barrier()
; #define PG8_SCHED __builtin_amdgcn_sched_barrier(0)
; template <class Epi, class Sched, bool ALIGN_EPI = false, bool SP2 = false, bool F8 = false>
; __device__ __forceinline__ void gemm_phase(PG8_LAS unsigned char* lds, const Gemm g, const Sched& S, const Epi& E) {
;     ...
;             PG8_LDB(B0, 1, 0); PG8_LDB(B1, 1, 1); PG8_SCHED; PG8_LDA(At, 1, 0); PG8_STAGE(PG8_SA(0, 1), a2 + hstep, voffA);
;             PG8_WAIT_V(8); PG8_WAIT_L(0); PG8_BAR; PG8_MMA(0, 0, At, B0); PG8_MMA(0, 1, At, B1); PG8_BAR; PG8_SCHED;
;             PG8_LDA(At, 1, 1); PG8_STAGE(PG8_SB(1, 0), b3, voffB); PG8_STAGE(PG8_SB(1, 1), b3 + hstep, voffB); PG8_STAGE(PG8_SA(1, 0), a3, voffA);
;             PG8_WAIT_V(8); PG8_WAIT_L(0); PG8_BAR; PG8_MMA(1, 0, At, B0); PG8_MMA(1, 1, At, B1); PG8_BAR; PG8_SCHED;
	ds_read_b128 v[2:5], v196
	ds_read_b128 v[6:9], v196 offset:1024
	ds_read_b128 v[10:13], v196 offset:2048
	ds_read_b128 v[14:17], v196 offset:3072
	ds_read_b128 v[18:21], v197
	ds_read_b128 v[22:25], v197 offset:1024
	ds_read_b128 v[26:29], v197 offset:2048
	ds_read_b128 v[30:33], v197 offset:3072
	s_add_u32 s4, s38, 0x70000
	s_addc_u32 s5, s39, 0
	s_mov_b32 m0, s47
	v_lshl_add_u64 v[232:233], s[4:5], 0, v[164:165]
	ds_read_b128 v[200:203], v194 offset:32768
	ds_read_b128 v[204:207], v194 offset:33792
	ds_read_b128 v[208:211], v194 offset:34816
	ds_read_b128 v[212:215], v194 offset:35840
	ds_read_b128 v[216:219], v194 offset:36864
	ds_read_b128 v[220:223], v194 offset:37888
	ds_read_b128 v[224:227], v194 offset:38912
	ds_read_b128 v[228:231], v194 offset:39936
	global_load_lds_dwordx4 v[232:233], off
	v_lshl_add_u64 v[232:233], s[4:5], 0, v[168:169]
	s_mov_b32 m0, s48
	s_nop 0
	global_load_lds_dwordx4 v[232:233], off
	s_waitcnt vmcnt(8)
	s_waitcnt lgkmcnt(0)
	s_barrier
	s_setprio 3
	s_waitcnt lgkmcnt(0)
	v_mfma_scale_f32_16x16x128_f8f6f4 v[158:161], v[2:9], v[200:207], v[158:161], v195, v195 op_sel_hi:[0,0,0]
	v_mfma_scale_f32_16x16x128_f8f6f4 v[154:157], v[10:17], v[200:207], v[154:157], v195, v195 op_sel_hi:[0,0,0]
	v_mfma_scale_f32_16x16x128_f8f6f4 v[142:145], v[2:9], v[208:215], v[142:145], v195, v195 op_sel_hi:[0,0,0]
	v_mfma_scale_f32_16x16x128_f8f6f4 v[138:141], v[10:17], v[208:215], v[138:141], v195, v195 op_sel_hi:[0,0,0]
	v_mfma_scale_f32_16x16x128_f8f6f4 v[126:129], v[2:9], v[216:223], v[126:129], v195, v195 op_sel_hi:[0,0,0]
	v_mfma_scale_f32_16x16x128_f8f6f4 v[122:125], v[10:17], v[216:223], v[122:125], v195, v195 op_sel_hi:[0,0,0]
	v_mfma_scale_f32_16x16x128_f8f6f4 v[110:113], v[2:9], v[224:231], v[110:113], v195, v195 op_sel_hi:[0,0,0]
	v_mfma_scale_f32_16x16x128_f8f6f4 v[106:109], v[10:17], v[224:231], v[106:109], v195, v195 op_sel_hi:[0,0,0]
	s_setprio 0
	s_setprio 3
	v_mfma_scale_f32_16x16x128_f8f6f4 v[150:153], v[18:25], v[200:207], v[150:153], v195, v195 op_sel_hi:[0,0,0]
	v_mfma_scale_f32_16x16x128_f8f6f4 v[146:149], v[26:33], v[200:207], v[146:149], v195, v195 op_sel_hi:[0,0,0]
	v_mfma_scale_f32_16x16x128_f8f6f4 v[134:137], v[18:25], v[208:215], v[134:137], v195, v195 op_sel_hi:[0,0,0]
	v_mfma_scale_f32_16x16x128_f8f6f4 v[130:133], v[26:33], v[208:215], v[130:133], v195, v195 op_sel_hi:[0,0,0]
	v_mfma_scale_f32_16x16x128_f8f6f4 v[118:121], v[18:25], v[216:223], v[118:121], v195, v195 op_sel_hi:[0,0,0]
	v_mfma_scale_f32_16x16x128_f8f6f4 v[114:117], v[26:33], v[216:223], v[114:117], v195, v195 op_sel_hi:[0,0,0]
	v_mfma_scale_f32_16x16x128_f8f6f4 v[102:105], v[18:25], v[224:231], v[102:105], v195, v195 op_sel_hi:[0,0,0]
	v_mfma_scale_f32_16x16x128_f8f6f4 v[98:101], v[26:33], v[224:231], v[98:101], v195, v195 op_sel_hi:[0,0,0]
	s_setprio 0
	s_barrier
	s_mov_b32 m0, s67
	v_lshl_add_u64 v[184:185], v[184:185], 0, s[18:19]
	ds_read_b128 v[200:203], v194 offset:49152
	ds_read_b128 v[204:207], v194 offset:50176
	ds_read_b128 v[208:211], v194 offset:51200
	ds_read_b128 v[212:215], v194 offset:52224
	ds_read_b128 v[216:219], v194 offset:53248
	ds_read_b128 v[220:223], v194 offset:54272
	ds_read_b128 v[224:227], v194 offset:55296
	ds_read_b128 v[228:231], v194 offset:56320
	global_load_lds_dwordx4 v[184:185], off
	v_lshl_add_u64 v[184:185], v[186:187], 0, s[18:19]
	s_mov_b32 m0, s70
	v_lshl_add_u64 v[182:183], v[182:183], 0, s[20:21]
	global_load_lds_dwordx4 v[184:185], off
	v_lshl_add_u64 v[184:185], v[182:183], 0, v[166:167]
	s_mov_b32 m0, s71
	v_lshl_add_u64 v[182:183], v[182:183], 0, v[170:171]
	global_load_lds_dwordx4 v[184:185], off
	s_mov_b32 m0, s72
	s_nop 0
	global_load_lds_dwordx4 v[182:183], off
	v_lshl_add_u64 v[182:183], v[188:189], 0, s[18:19]
	s_mov_b32 m0, s49
	s_nop 0
	global_load_lds_dwordx4 v[182:183], off
	v_lshl_add_u64 v[182:183], v[190:191], 0, s[18:19]
	s_mov_b32 m0, s50
	s_nop 0
	global_load_lds_dwordx4 v[182:183], off
	s_waitcnt vmcnt(8)
	s_waitcnt lgkmcnt(0)
	s_barrier
	s_setprio 3
	s_waitcnt lgkmcnt(0)
	v_mfma_scale_f32_16x16x128_f8f6f4 v[94:97], v[2:9], v[200:207], v[94:97], v195, v195 op_sel_hi:[0,0,0]
	v_mfma_scale_f32_16x16x128_f8f6f4 v[90:93], v[10:17], v[200:207], v[90:93], v195, v195 op_sel_hi:[0,0,0]
	v_mfma_scale_f32_16x16x128_f8f6f4 v[78:81], v[2:9], v[208:215], v[78:81], v195, v195 op_sel_hi:[0,0,0]
	v_mfma_scale_f32_16x16x128_f8f6f4 v[74:77], v[10:17], v[208:215], v[74:77], v195, v195 op_sel_hi:[0,0,0]
	v_mfma_scale_f32_16x16x128_f8f6f4 v[62:65], v[2:9], v[216:223], v[62:65], v195, v195 op_sel_hi:[0,0,0]
	v_mfma_scale_f32_16x16x128_f8f6f4 v[58:61], v[10:17], v[216:223], v[58:61], v195, v195 op_sel_hi:[0,0,0]
	v_mfma_scale_f32_16x16x128_f8f6f4 v[46:49], v[2:9], v[224:231], v[46:49], v195, v195 op_sel_hi:[0,0,0]
	v_mfma_scale_f32_16x16x128_f8f6f4 v[42:45], v[10:17], v[224:231], v[42:45], v195, v195 op_sel_hi:[0,0,0]
	s_setprio 0
	s_setprio 3
	v_mfma_scale_f32_16x16x128_f8f6f4 v[86:89], v[18:25], v[200:207], v[86:89], v195, v195 op_sel_hi:[0,0,0]
	v_mfma_scale_f32_16x16x128_f8f6f4 v[82:85], v[26:33], v[200:207], v[82:85], v195, v195 op_sel_hi:[0,0,0]
	v_mfma_scale_f32_16x16x128_f8f6f4 v[70:73], v[18:25], v[208:215], v[70:73], v195, v195 op_sel_hi:[0,0,0]
	v_mfma_scale_f32_16x16x128_f8f6f4 v[66:69], v[26:33], v[208:215], v[66:69], v195, v195 op_sel_hi:[0,0,0]
	v_mfma_scale_f32_16x16x128_f8f6f4 v[54:57], v[18:25], v[216:223], v[54:57], v195, v195 op_sel_hi:[0,0,0]
	v_mfma_scale_f32_16x16x128_f8f6f4 v[50:53], v[26:33], v[216:223], v[50:53], v195, v195 op_sel_hi:[0,0,0]
	v_mfma_scale_f32_16x16x128_f8f6f4 v[38:41], v[18:25], v[224:231], v[38:41], v195, v195 op_sel_hi:[0,0,0]
	v_mfma_scale_f32_16x16x128_f8f6f4 v[34:37], v[26:33], v[224:231], v[34:37], v195, v195 op_sel_hi:[0,0,0]
	s_setprio 0
	s_barrier
	s_add_i32 s76, s76, 2
	v_lshl_add_u64 v[180:181], v[180:181], 0, s[24:25]
	s_cmp_gt_u32 s76, 25
	s_mov_b64 s[36:37], s[30:31]
	s_cbranch_scc1 .Lpeel_exit_4

; __global__ void __launch_bounds__(NTHREADS, 2) fwd(Args args) {
	.amdhsa_kernel _Z3fwd4Args
		.amdhsa_group_segment_fixed_size 0
		.amdhsa_private_segment_fixed_size 0
		.amdhsa_kernarg_size 448
		.amdhsa_user_sgpr_count 2
		.amdhsa_user_sgpr_dispatch_ptr 0
		.amdhsa_user_sgpr_queue_ptr 0
		.amdhsa_user_sgpr_kernarg_segment_ptr 1
		.amdhsa_user_sgpr_dispatch_id 0
		.amdhsa_user_sgpr_kernarg_preload_length 0
		.amdhsa_user_sgpr_kernarg_preload_offset 0
		.amdhsa_user_sgpr_private_segment_size 0
		.amdhsa_uses_dynamic_stack 0
		.amdhsa_enable_private_segment 0
		.amdhsa_system_sgpr_workgroup_id_x 1
		.amdhsa_system_sgpr_workgroup_id_y 0
		.amdhsa_system_sgpr_workgroup_id_z 0
		.amdhsa_system_sgpr_workgroup_info 0
		.amdhsa_system_vgpr_workitem_id 0
		.amdhsa_next_free_vgpr 249
		.amdhsa_next_free_sgpr 100
		.amdhsa_accum_offset 252
		.amdhsa_reserve_vcc 1
		.amdhsa_float_round_mode_32 0
		.amdhsa_float_round_mode_16_64 0
		.amdhsa_float_denorm_mode_32 3
		.amdhsa_float_denorm_mode_16_64 3
		.amdhsa_dx10_clamp 1
		.amdhsa_ieee_mode 1
		.amdhsa_fp16_overflow 0
		.amdhsa_tg_split 0
		.amdhsa_exception_fp_ieee_invalid_op 0
		.amdhsa_exception_fp_denorm_src 0
		.amdhsa_exception_fp_ieee_div_zero 0
		.amdhsa_exception_fp_ieee_overflow 0
		.amdhsa_exception_fp_ieee_underflow 0
		.amdhsa_exception_fp_ieee_inexact 0
		.amdhsa_exception_int_div_zero 0
	.end_amdhsa_kernel

; __global__ void __launch_bounds__(NTHREADS, 2) fwd(Args args) {
amdhsa.kernels:
  - .agpr_count:     0
    .args:
      - .offset:         0
        .size:           192
        .value_kind:     by_value
      - .offset:         192
        .size:           4
        .value_kind:     hidden_block_count_x
      - .offset:         196
        .size:           4
        .value_kind:     hidden_block_count_y
      - .offset:         200
        .size:           4
        .value_kind:     hidden_block_count_z
      - .offset:         204
        .size:           2
        .value_kind:     hidden_group_size_x
      - .offset:         206
        .size:           2
        .value_kind:     hidden_group_size_y
      - .offset:         208
        .size:           2
        .value_kind:     hidden_group_size_z
      - .offset:         210
        .size:           2
        .value_kind:     hidden_remainder_x
      - .offset:         212
        .size:           2
        .value_kind:     hidden_remainder_y
      - .offset:         214
        .size:           2
        .value_kind:     hidden_remainder_z
      - .offset:         232
        .size:           8
        .value_kind:     hidden_global_offset_x
      - .offset:         240
        .size:           8
        .value_kind:     hidden_global_offset_y
      - .offset:         248
        .size:           8
        .value_kind:     hidden_global_offset_z
      - .offset:         256
        .size:           2
        .value_kind:     hidden_grid_dims
      - .offset:         312
        .size:           4
        .value_kind:     hidden_dynamic_lds_size
    .group_segment_fixed_size: 0
    .kernarg_segment_align: 8
    .kernarg_segment_size: 448
    .language:       OpenCL C
    .language_version:
      - 2
      - 0
    .max_flat_workgroup_size: 512
    .name:           _Z3fwd4Args
    .private_segment_fixed_size: 0
    .sgpr_count:     106
    .sgpr_spill_count: 10
    .symbol:         _Z3fwd4Args.kd
    .uniform_work_group_size: 1
    .uses_dynamic_stack: false
    .vgpr_count:     249
    .vgpr_spill_count: 0
    .wavefront_size: 64
